# P6: cache-line touch loads issued up front for the mid-K rescale groups and for the 16 epilogue gate loads so their misses overlap
# baseline (speedup 1.0000x reference)
.LBB0_971:
	s_cmp_lg_u32 s71, 2
	s_cselect_b64 s[40:41], -1, 0
	s_and_b64 s[40:41], s[40:41], s[36:37]
	s_andn2_b64 vcc, exec, s[40:41]
	s_cbranch_vccnz .LBB0_964
	s_cmp_eq_u32 s71, 0
	v_mov_b32_e32 v3, v134
	v_mov_b64_e32 v[136:137], s[8:9]
	s_cselect_b64 vcc, -1, 0
	s_and_b64 s[40:41], vcc, exec
	v_mad_i64_i32 v[4:5], s[42:43], v3, s64, v[136:137]
	v_lshl_add_u64 v[234:235], v[4:5], 0, s[16:17]
	v_lshlrev_b64 v[166:167], 1, v[148:149]
	s_cselect_b32 s0, 0, 0x800
	v_lshl_add_u64 v[4:5], v[234:235], 0, v[166:167]
	s_cselect_b32 s40, 0x800, s63
	s_mov_b32 s41, s1
	v_lshl_add_u64 v[226:227], v[4:5], 0, s[0:1]
	v_lshl_add_u64 v[4:5], v[4:5], 0, s[40:41]
	global_load_dwordx4 v[226:229], v[226:227], off
	s_nop 0
	global_load_dwordx4 v[230:233], v[4:5], off
	v_lshl_add_u64 v[236:237], v[234:235], 0, s[0:1]
	v_lshlrev_b64 v[4:5], 1, v[150:151]
	v_lshl_add_u64 v[234:235], v[234:235], 0, s[40:41]
	v_lshl_add_u64 v[236:237], v[236:237], 0, v[4:5]
	v_lshl_add_u64 v[238:239], v[234:235], 0, v[4:5]
	global_load_dwordx4 v[234:237], v[236:237], off
	s_nop 0
	global_load_dwordx4 v[238:241], v[238:239], off
	v_mad_i64_i32 v[188:189], s[42:43], v162, s64, v[136:137]
	v_lshl_add_u64 v[188:189], v[188:189], 0, s[16:17]
	v_lshl_add_u64 v[190:191], v[188:189], 0, v[166:167]
	v_lshl_add_u64 v[192:193], v[190:191], 0, s[40:41]
	global_load_dword v213, v[192:193], off
	v_lshl_add_u64 v[190:191], v[190:191], 0, s[0:1]
	global_load_dword v213, v[190:191], off
	v_lshl_add_u64 v[188:189], v[188:189], 0, v[4:5]
	v_lshl_add_u64 v[192:193], v[188:189], 0, s[40:41]
	global_load_dword v213, v[192:193], off
	v_lshl_add_u64 v[188:189], v[188:189], 0, s[0:1]
	global_load_dword v213, v[188:189], off
	v_mad_i64_i32 v[188:189], s[42:43], v160, s64, v[136:137]
	v_lshl_add_u64 v[188:189], v[188:189], 0, s[16:17]
	v_lshl_add_u64 v[190:191], v[188:189], 0, v[166:167]
	v_lshl_add_u64 v[192:193], v[190:191], 0, s[40:41]
	global_load_dword v213, v[192:193], off
	v_lshl_add_u64 v[190:191], v[190:191], 0, s[0:1]
	global_load_dword v213, v[190:191], off
	v_lshl_add_u64 v[188:189], v[188:189], 0, v[4:5]
	v_lshl_add_u64 v[192:193], v[188:189], 0, s[40:41]
	global_load_dword v213, v[192:193], off
	v_lshl_add_u64 v[188:189], v[188:189], 0, s[0:1]
	global_load_dword v213, v[188:189], off
	v_mad_i64_i32 v[188:189], s[42:43], v158, s64, v[136:137]
	v_lshl_add_u64 v[188:189], v[188:189], 0, s[16:17]
	v_lshl_add_u64 v[190:191], v[188:189], 0, v[166:167]
	v_lshl_add_u64 v[192:193], v[190:191], 0, s[40:41]
	global_load_dword v213, v[192:193], off
	v_lshl_add_u64 v[190:191], v[190:191], 0, s[0:1]
	global_load_dword v213, v[190:191], off
	v_lshl_add_u64 v[188:189], v[188:189], 0, v[4:5]
	v_lshl_add_u64 v[192:193], v[188:189], 0, s[40:41]
	global_load_dword v213, v[192:193], off
	v_lshl_add_u64 v[188:189], v[188:189], 0, s[0:1]
	global_load_dword v213, v[188:189], off
	v_mad_i64_i32 v[188:189], s[42:43], v156, s64, v[136:137]
	v_lshl_add_u64 v[188:189], v[188:189], 0, s[16:17]
	v_lshl_add_u64 v[190:191], v[188:189], 0, v[166:167]
	v_lshl_add_u64 v[192:193], v[190:191], 0, s[40:41]
	global_load_dword v213, v[192:193], off
	v_lshl_add_u64 v[190:191], v[190:191], 0, s[0:1]
	global_load_dword v213, v[190:191], off
	v_lshl_add_u64 v[188:189], v[188:189], 0, v[4:5]
	v_lshl_add_u64 v[192:193], v[188:189], 0, s[40:41]
	global_load_dword v213, v[192:193], off
	v_lshl_add_u64 v[188:189], v[188:189], 0, s[0:1]
	global_load_dword v213, v[188:189], off
	v_mad_i64_i32 v[188:189], s[42:43], v154, s64, v[136:137]
	v_lshl_add_u64 v[188:189], v[188:189], 0, s[16:17]
	v_lshl_add_u64 v[190:191], v[188:189], 0, v[166:167]
	v_lshl_add_u64 v[192:193], v[190:191], 0, s[40:41]
	global_load_dword v213, v[192:193], off
	v_lshl_add_u64 v[190:191], v[190:191], 0, s[0:1]
	global_load_dword v213, v[190:191], off
	v_lshl_add_u64 v[188:189], v[188:189], 0, v[4:5]
	v_lshl_add_u64 v[192:193], v[188:189], 0, s[40:41]
	global_load_dword v213, v[192:193], off
	v_lshl_add_u64 v[188:189], v[188:189], 0, s[0:1]
	global_load_dword v213, v[188:189], off
	v_mad_i64_i32 v[188:189], s[42:43], v152, s64, v[136:137]
	v_lshl_add_u64 v[188:189], v[188:189], 0, s[16:17]
	v_lshl_add_u64 v[190:191], v[188:189], 0, v[166:167]
	v_lshl_add_u64 v[192:193], v[190:191], 0, s[40:41]
	global_load_dword v213, v[192:193], off
	v_lshl_add_u64 v[190:191], v[190:191], 0, s[0:1]
	global_load_dword v213, v[190:191], off
	v_lshl_add_u64 v[188:189], v[188:189], 0, v[4:5]
	v_lshl_add_u64 v[192:193], v[188:189], 0, s[40:41]
	global_load_dword v213, v[192:193], off
	v_lshl_add_u64 v[188:189], v[188:189], 0, s[0:1]
	global_load_dword v213, v[188:189], off
	v_mov_b32_e32 v3, v164
	s_nop 0
	v_mad_i64_i32 v[168:169], s[42:43], v3, s64, v[136:137]
	v_lshl_add_u64 v[180:181], v[168:169], 0, s[16:17]
	v_lshl_add_u64 v[168:169], v[180:181], 0, v[166:167]
	v_lshl_add_u64 v[170:171], v[168:169], 0, s[0:1]
	v_lshl_add_u64 v[176:177], v[168:169], 0, s[40:41]
	global_load_dwordx4 v[168:171], v[170:171], off
	s_nop 0
	global_load_dwordx4 v[176:179], v[176:177], off
	v_lshl_add_u64 v[184:185], v[180:181], 0, s[0:1]
	v_lshl_add_u64 v[180:181], v[180:181], 0, s[40:41]
	v_lshl_add_u64 v[180:181], v[180:181], 0, v[4:5]
	global_load_dwordx4 v[180:183], v[180:181], off
	v_lshl_add_u64 v[184:185], v[184:185], 0, v[4:5]
	global_load_dwordx4 v[184:187], v[184:185], off
	s_waitcnt vmcnt(4)
	v_cvt_f32_f16_e32 v3, v226
	v_cvt_f32_f16_e32 v135, v230
	v_cvt_f32_f16_sdwa v155, v230 dst_sel:DWORD dst_unused:UNUSED_PAD src0_sel:WORD_1
	v_cvt_f32_f16_e32 v159, v231
	v_cvt_f32_f16_sdwa v153, v226 dst_sel:DWORD dst_unused:UNUSED_PAD src0_sel:WORD_1
	v_max_f32_e32 v135, 0x38d1b717, v135
	v_rcp_f32_e32 v135, v135
	v_cvt_f32_f16_e32 v157, v227
	v_max_f32_e32 v188, 0x38d1b717, v3
	v_max_f32_e32 v155, 0x38d1b717, v155
	v_max_f32_e32 v159, 0x38d1b717, v159
	v_cndmask_b32_e32 v3, v188, v3, vcc
	v_rcp_f32_e32 v155, v155
	v_cvt_f32_f16_sdwa v163, v231 dst_sel:DWORD dst_unused:UNUSED_PAD src0_sel:WORD_1
	v_cvt_f32_f16_e32 v230, v233
	v_cvt_f32_f16_sdwa v231, v233 dst_sel:DWORD dst_unused:UNUSED_PAD src0_sel:WORD_1
	v_cvt_f32_f16_e32 v233, v238
	v_cvt_f32_f16_sdwa v238, v238 dst_sel:DWORD dst_unused:UNUSED_PAD src0_sel:WORD_1
	v_rcp_f32_e32 v159, v159
	v_mul_f32_e32 v3, v3, v135
	v_max_f32_e32 v189, 0x38d1b717, v153
	v_mul_f32_e32 v130, v130, v3
	v_cvt_f32_f16_sdwa v3, v234 dst_sel:DWORD dst_unused:UNUSED_PAD src0_sel:WORD_1
	v_max_f32_e32 v190, 0x38d1b717, v157
	v_cndmask_b32_e32 v153, v189, v153, vcc
	v_cndmask_b32_e32 v157, v190, v157, vcc
	v_mul_f32_e32 v135, v153, v155
	v_mul_f32_e32 v153, v157, v159
	v_mul_f32_e32 v131, v131, v135
	v_max_f32_e32 v135, 0x38d1b717, v238
	v_mul_f32_e32 v132, v132, v153
	v_rcp_f32_e32 v135, v135
	v_max_f32_e32 v153, 0x38d1b717, v3
	v_cndmask_b32_e32 v3, v153, v3, vcc
	v_cvt_f32_f16_e32 v153, v239
	v_mul_f32_e32 v3, v3, v135
	v_cvt_f32_f16_e32 v135, v235
	v_mul_f32_e32 v123, v123, v3
	v_max_f32_e32 v3, 0x38d1b717, v153
	v_rcp_f32_e32 v3, v3
	v_max_f32_e32 v153, 0x38d1b717, v135
	v_cndmask_b32_e32 v135, v153, v135, vcc
	v_cvt_f32_f16_sdwa v153, v239 dst_sel:DWORD dst_unused:UNUSED_PAD src0_sel:WORD_1
	v_mul_f32_e32 v3, v135, v3
	v_cvt_f32_f16_sdwa v135, v235 dst_sel:DWORD dst_unused:UNUSED_PAD src0_sel:WORD_1
	v_mul_f32_e32 v124, v124, v3
	v_max_f32_e32 v3, 0x38d1b717, v153
	v_rcp_f32_e32 v3, v3
	v_max_f32_e32 v153, 0x38d1b717, v135
	v_cndmask_b32_e32 v135, v153, v135, vcc
	v_cvt_f32_f16_e32 v153, v240
	v_mul_f32_e32 v3, v135, v3
	v_cvt_f32_f16_e32 v135, v236
	v_mul_f32_e32 v125, v125, v3
	v_max_f32_e32 v3, 0x38d1b717, v153
	v_rcp_f32_e32 v3, v3
	v_max_f32_e32 v153, 0x38d1b717, v135
	v_cndmask_b32_e32 v135, v153, v135, vcc
	v_cvt_f32_f16_sdwa v153, v240 dst_sel:DWORD dst_unused:UNUSED_PAD src0_sel:WORD_1
	v_mul_f32_e32 v3, v135, v3
	v_cvt_f32_f16_sdwa v135, v236 dst_sel:DWORD dst_unused:UNUSED_PAD src0_sel:WORD_1
	v_mul_f32_e32 v118, v118, v3
	v_max_f32_e32 v3, 0x38d1b717, v153
	v_cvt_f32_f16_sdwa v161, v227 dst_sel:DWORD dst_unused:UNUSED_PAD src0_sel:WORD_1
	v_rcp_f32_e32 v3, v3
	v_max_f32_e32 v153, 0x38d1b717, v135
	v_max_f32_e32 v163, 0x38d1b717, v163
	v_cndmask_b32_e32 v135, v153, v135, vcc
	v_cvt_f32_f16_e32 v153, v241
	v_rcp_f32_e32 v163, v163
	v_max_f32_e32 v191, 0x38d1b717, v161
	v_mul_f32_e32 v3, v135, v3
	v_cvt_f32_f16_e32 v135, v237
	v_cndmask_b32_e32 v161, v191, v161, vcc
	v_mul_f32_e32 v119, v119, v3
	v_max_f32_e32 v3, 0x38d1b717, v153
	v_mul_f32_e32 v155, v161, v163
	v_rcp_f32_e32 v3, v3
	v_cvt_f32_f16_e32 v165, v228
	v_cvt_f32_f16_e32 v226, v232
	v_cvt_f32_f16_sdwa v227, v228 dst_sel:DWORD dst_unused:UNUSED_PAD src0_sel:WORD_1
	v_cvt_f32_f16_sdwa v228, v232 dst_sel:DWORD dst_unused:UNUSED_PAD src0_sel:WORD_1
	v_mul_f32_e32 v133, v133, v155
	v_cvt_f32_f16_sdwa v155, v241 dst_sel:DWORD dst_unused:UNUSED_PAD src0_sel:WORD_1
	v_max_f32_e32 v153, 0x38d1b717, v135
	v_cndmask_b32_e32 v135, v153, v135, vcc
	v_cvt_f32_f16_e32 v175, v229
	v_cvt_f32_f16_sdwa v229, v229 dst_sel:DWORD dst_unused:UNUSED_PAD src0_sel:WORD_1
	v_cvt_f32_f16_e32 v232, v234
	v_mul_f32_e32 v3, v135, v3
	v_cvt_f32_f16_sdwa v135, v237 dst_sel:DWORD dst_unused:UNUSED_PAD src0_sel:WORD_1
	v_max_f32_e32 v226, 0x38d1b717, v226
	v_max_f32_e32 v228, 0x38d1b717, v228
	v_max_f32_e32 v230, 0x38d1b717, v230
	v_max_f32_e32 v231, 0x38d1b717, v231
	v_max_f32_e32 v233, 0x38d1b717, v233
	v_max_f32_e32 v153, 0x38d1b717, v155
	v_rcp_f32_e32 v226, v226
	v_rcp_f32_e32 v228, v228
	v_rcp_f32_e32 v230, v230
	v_rcp_f32_e32 v231, v231
	v_rcp_f32_e32 v233, v233
	v_rcp_f32_e32 v153, v153
	v_max_f32_e32 v192, 0x38d1b717, v165
	v_max_f32_e32 v193, 0x38d1b717, v227
	v_max_f32_e32 v194, 0x38d1b717, v175
	v_max_f32_e32 v195, 0x38d1b717, v229
	v_max_f32_e32 v196, 0x38d1b717, v232
	v_mul_f32_e32 v120, v120, v3
	v_max_f32_e32 v3, 0x38d1b717, v135
	v_cndmask_b32_e32 v165, v192, v165, vcc
	v_cndmask_b32_e32 v227, v193, v227, vcc
	v_cndmask_b32_e32 v175, v194, v175, vcc
	v_cndmask_b32_e32 v229, v195, v229, vcc
	v_cndmask_b32_e32 v232, v196, v232, vcc
	v_cndmask_b32_e32 v3, v3, v135, vcc
	v_mul_f32_e32 v157, v165, v226
	v_mul_f32_e32 v159, v227, v228
	v_mul_f32_e32 v161, v175, v230
	v_mul_f32_e32 v163, v229, v231
	v_mul_f32_e32 v165, v232, v233
	v_mul_f32_e32 v3, v3, v153
	v_mul_f32_e32 v126, v126, v157
	v_mul_f32_e32 v127, v127, v159
	v_mul_f32_e32 v128, v128, v161
	v_mul_f32_e32 v129, v129, v163
	v_mul_f32_e32 v122, v122, v165
	v_mul_f32_e32 v121, v121, v3
	v_mov_b32_e32 v3, v162
	s_nop 0
	v_mad_i64_i32 v[226:227], s[42:43], v3, s64, v[136:137]
	v_lshl_add_u64 v[234:235], v[226:227], 0, s[16:17]
	v_lshl_add_u64 v[230:231], v[234:235], 0, v[166:167]
	v_lshl_add_u64 v[226:227], v[230:231], 0, s[40:41]
	global_load_dwordx4 v[226:229], v[226:227], off
	v_lshl_add_u64 v[230:231], v[230:231], 0, s[0:1]
	global_load_dwordx4 v[230:233], v[230:231], off
	v_lshl_add_u64 v[238:239], v[234:235], 0, s[0:1]
	v_lshl_add_u64 v[234:235], v[234:235], 0, s[40:41]
	v_lshl_add_u64 v[234:235], v[234:235], 0, v[4:5]
	global_load_dwordx4 v[234:237], v[234:235], off
	v_lshl_add_u64 v[238:239], v[238:239], 0, v[4:5]
	global_load_dwordx4 v[238:241], v[238:239], off
	s_waitcnt vmcnt(4)
	v_cvt_f32_f16_e32 v3, v168
	v_cvt_f32_f16_e32 v135, v176
	v_cvt_f32_f16_sdwa v155, v176 dst_sel:DWORD dst_unused:UNUSED_PAD src0_sel:WORD_1
	v_cvt_f32_f16_sdwa v153, v168 dst_sel:DWORD dst_unused:UNUSED_PAD src0_sel:WORD_1
	v_cvt_f32_f16_e32 v159, v177
	v_max_f32_e32 v135, 0x38d1b717, v135
	v_max_f32_e32 v155, 0x38d1b717, v155
	v_rcp_f32_e32 v135, v135
	v_rcp_f32_e32 v155, v155
	v_cvt_f32_f16_e32 v157, v169
	v_max_f32_e32 v163, 0x38d1b717, v3
	v_max_f32_e32 v165, 0x38d1b717, v153
	v_max_f32_e32 v159, 0x38d1b717, v159
	v_cndmask_b32_e32 v3, v163, v3, vcc
	v_cndmask_b32_e32 v153, v165, v153, vcc
	v_rcp_f32_e32 v159, v159
	v_cvt_f32_f16_sdwa v161, v177 dst_sel:DWORD dst_unused:UNUSED_PAD src0_sel:WORD_1
	v_mul_f32_e32 v3, v3, v135
	v_mul_f32_e32 v135, v153, v155
	v_max_f32_e32 v168, 0x38d1b717, v157
	v_mul_f32_e32 v115, v115, v135
	v_cvt_f32_f16_sdwa v135, v169 dst_sel:DWORD dst_unused:UNUSED_PAD src0_sel:WORD_1
	v_cndmask_b32_e32 v157, v168, v157, vcc
	v_mul_f32_e32 v114, v114, v3
	v_mul_f32_e32 v3, v157, v159
	v_mul_f32_e32 v116, v116, v3
	v_max_f32_e32 v3, 0x38d1b717, v161
	v_rcp_f32_e32 v3, v3
	v_max_f32_e32 v153, 0x38d1b717, v135
	v_cndmask_b32_e32 v135, v153, v135, vcc
	v_cvt_f32_f16_e32 v153, v178
	v_mul_f32_e32 v3, v135, v3
	v_cvt_f32_f16_e32 v135, v170
	v_mul_f32_e32 v117, v117, v3
	v_max_f32_e32 v3, 0x38d1b717, v153
	v_rcp_f32_e32 v3, v3
	v_max_f32_e32 v153, 0x38d1b717, v135
	v_cndmask_b32_e32 v135, v153, v135, vcc
	v_cvt_f32_f16_sdwa v153, v178 dst_sel:DWORD dst_unused:UNUSED_PAD src0_sel:WORD_1
	v_mul_f32_e32 v3, v135, v3
	v_cvt_f32_f16_sdwa v135, v170 dst_sel:DWORD dst_unused:UNUSED_PAD src0_sel:WORD_1
	v_mul_f32_e32 v110, v110, v3
	v_max_f32_e32 v3, 0x38d1b717, v153
	v_rcp_f32_e32 v3, v3
	v_max_f32_e32 v153, 0x38d1b717, v135
	v_cndmask_b32_e32 v135, v153, v135, vcc
	v_cvt_f32_f16_e32 v153, v179
	v_mul_f32_e32 v3, v135, v3
	v_cvt_f32_f16_e32 v135, v171
	v_mul_f32_e32 v111, v111, v3
	v_max_f32_e32 v3, 0x38d1b717, v153
	v_rcp_f32_e32 v3, v3
	v_max_f32_e32 v153, 0x38d1b717, v135
	v_cndmask_b32_e32 v135, v153, v135, vcc
	v_cvt_f32_f16_sdwa v153, v179 dst_sel:DWORD dst_unused:UNUSED_PAD src0_sel:WORD_1
	v_mul_f32_e32 v3, v135, v3
	v_cvt_f32_f16_sdwa v135, v171 dst_sel:DWORD dst_unused:UNUSED_PAD src0_sel:WORD_1
	v_mul_f32_e32 v112, v112, v3
	v_max_f32_e32 v3, 0x38d1b717, v153
	v_rcp_f32_e32 v3, v3
	v_max_f32_e32 v153, 0x38d1b717, v135
	v_cndmask_b32_e32 v135, v153, v135, vcc
	v_cvt_f32_f16_e32 v153, v180
	v_mul_f32_e32 v3, v135, v3
	v_cvt_f32_f16_e32 v135, v184
	v_mul_f32_e32 v113, v113, v3
	v_max_f32_e32 v3, 0x38d1b717, v153
	v_rcp_f32_e32 v3, v3
	v_max_f32_e32 v153, 0x38d1b717, v135
	v_cndmask_b32_e32 v135, v153, v135, vcc
	v_cvt_f32_f16_sdwa v153, v180 dst_sel:DWORD dst_unused:UNUSED_PAD src0_sel:WORD_1
	v_mul_f32_e32 v3, v135, v3
	v_cvt_f32_f16_sdwa v135, v184 dst_sel:DWORD dst_unused:UNUSED_PAD src0_sel:WORD_1
	v_mul_f32_e32 v106, v106, v3
	v_max_f32_e32 v3, 0x38d1b717, v153
	v_rcp_f32_e32 v3, v3
	v_max_f32_e32 v153, 0x38d1b717, v135
	v_cndmask_b32_e32 v135, v153, v135, vcc
	v_cvt_f32_f16_e32 v153, v181
	v_mul_f32_e32 v3, v135, v3
	v_cvt_f32_f16_e32 v135, v185
	v_mul_f32_e32 v107, v107, v3
	v_max_f32_e32 v3, 0x38d1b717, v153
	v_rcp_f32_e32 v3, v3
	v_max_f32_e32 v153, 0x38d1b717, v135
	v_cndmask_b32_e32 v135, v153, v135, vcc
	v_cvt_f32_f16_sdwa v153, v181 dst_sel:DWORD dst_unused:UNUSED_PAD src0_sel:WORD_1
	v_mul_f32_e32 v3, v135, v3
	v_cvt_f32_f16_sdwa v135, v185 dst_sel:DWORD dst_unused:UNUSED_PAD src0_sel:WORD_1
	v_mul_f32_e32 v108, v108, v3
	v_max_f32_e32 v3, 0x38d1b717, v153
	v_rcp_f32_e32 v3, v3
	v_max_f32_e32 v153, 0x38d1b717, v135
	v_cndmask_b32_e32 v135, v153, v135, vcc
	v_cvt_f32_f16_e32 v153, v182
	v_mul_f32_e32 v3, v135, v3
	v_cvt_f32_f16_e32 v135, v186
	v_mul_f32_e32 v109, v109, v3
	v_max_f32_e32 v3, 0x38d1b717, v153
	v_rcp_f32_e32 v3, v3
	v_max_f32_e32 v153, 0x38d1b717, v135
	v_cndmask_b32_e32 v135, v153, v135, vcc
	v_cvt_f32_f16_sdwa v153, v182 dst_sel:DWORD dst_unused:UNUSED_PAD src0_sel:WORD_1
	v_mul_f32_e32 v3, v135, v3
	v_cvt_f32_f16_sdwa v135, v186 dst_sel:DWORD dst_unused:UNUSED_PAD src0_sel:WORD_1
	v_mul_f32_e32 v102, v102, v3
	v_max_f32_e32 v3, 0x38d1b717, v153
	v_rcp_f32_e32 v3, v3
	v_max_f32_e32 v153, 0x38d1b717, v135
	v_cndmask_b32_e32 v135, v153, v135, vcc
	v_cvt_f32_f16_e32 v153, v183
	v_mul_f32_e32 v3, v135, v3
	v_cvt_f32_f16_e32 v135, v187
	v_mul_f32_e32 v103, v103, v3
	v_max_f32_e32 v3, 0x38d1b717, v153
	v_rcp_f32_e32 v3, v3
	v_cvt_f32_f16_sdwa v155, v183 dst_sel:DWORD dst_unused:UNUSED_PAD src0_sel:WORD_1
	v_max_f32_e32 v153, 0x38d1b717, v135
	v_cndmask_b32_e32 v135, v153, v135, vcc
	v_mul_f32_e32 v3, v135, v3
	v_cvt_f32_f16_sdwa v135, v187 dst_sel:DWORD dst_unused:UNUSED_PAD src0_sel:WORD_1
	v_max_f32_e32 v153, 0x38d1b717, v155
	v_rcp_f32_e32 v153, v153
	v_mul_f32_e32 v104, v104, v3
	v_max_f32_e32 v3, 0x38d1b717, v135
	v_cndmask_b32_e32 v3, v3, v135, vcc
	v_mul_f32_e32 v3, v3, v153
	v_mul_f32_e32 v105, v105, v3
	v_mov_b32_e32 v3, v160
	s_nop 0
	v_mad_i64_i32 v[168:169], s[42:43], v3, s64, v[136:137]
	v_lshl_add_u64 v[180:181], v[168:169], 0, s[16:17]
	v_lshl_add_u64 v[176:177], v[180:181], 0, v[166:167]
	v_lshl_add_u64 v[168:169], v[176:177], 0, s[40:41]
	global_load_dwordx4 v[168:171], v[168:169], off
	v_lshl_add_u64 v[176:177], v[176:177], 0, s[0:1]
	global_load_dwordx4 v[176:179], v[176:177], off
	v_lshl_add_u64 v[184:185], v[180:181], 0, s[0:1]
	v_lshl_add_u64 v[180:181], v[180:181], 0, s[40:41]
	v_lshl_add_u64 v[180:181], v[180:181], 0, v[4:5]
	global_load_dwordx4 v[180:183], v[180:181], off
	v_lshl_add_u64 v[184:185], v[184:185], 0, v[4:5]
	global_load_dwordx4 v[184:187], v[184:185], off
	s_waitcnt vmcnt(4)
	v_cvt_f32_f16_e32 v3, v226
	v_cvt_f32_f16_e32 v135, v230
	v_max_f32_e32 v3, 0x38d1b717, v3
	v_rcp_f32_e32 v3, v3
	v_max_f32_e32 v153, 0x38d1b717, v135
	v_cndmask_b32_e32 v135, v153, v135, vcc
	v_cvt_f32_f16_sdwa v153, v226 dst_sel:DWORD dst_unused:UNUSED_PAD src0_sel:WORD_1
	v_mul_f32_e32 v3, v135, v3
	v_cvt_f32_f16_sdwa v135, v230 dst_sel:DWORD dst_unused:UNUSED_PAD src0_sel:WORD_1
	v_mul_f32_e32 v98, v98, v3
	v_max_f32_e32 v3, 0x38d1b717, v153
	v_rcp_f32_e32 v3, v3
	v_max_f32_e32 v153, 0x38d1b717, v135
	v_cndmask_b32_e32 v135, v153, v135, vcc
	v_cvt_f32_f16_e32 v153, v227
	v_mul_f32_e32 v3, v135, v3
	v_cvt_f32_f16_e32 v135, v231
	v_mul_f32_e32 v99, v99, v3
	v_max_f32_e32 v3, 0x38d1b717, v153
	v_rcp_f32_e32 v3, v3
	v_max_f32_e32 v153, 0x38d1b717, v135
	v_cndmask_b32_e32 v135, v153, v135, vcc
	v_cvt_f32_f16_sdwa v153, v227 dst_sel:DWORD dst_unused:UNUSED_PAD src0_sel:WORD_1
	v_mul_f32_e32 v3, v135, v3
	v_cvt_f32_f16_sdwa v135, v231 dst_sel:DWORD dst_unused:UNUSED_PAD src0_sel:WORD_1
	v_mul_f32_e32 v100, v100, v3
	v_max_f32_e32 v3, 0x38d1b717, v153
	v_rcp_f32_e32 v3, v3
	v_max_f32_e32 v153, 0x38d1b717, v135
	v_cndmask_b32_e32 v135, v153, v135, vcc
	v_cvt_f32_f16_e32 v153, v228
	v_mul_f32_e32 v3, v135, v3
	v_cvt_f32_f16_e32 v135, v232
	v_mul_f32_e32 v101, v101, v3
	v_max_f32_e32 v3, 0x38d1b717, v153
	v_rcp_f32_e32 v3, v3
	v_max_f32_e32 v153, 0x38d1b717, v135
	v_cndmask_b32_e32 v135, v153, v135, vcc
	v_cvt_f32_f16_sdwa v153, v228 dst_sel:DWORD dst_unused:UNUSED_PAD src0_sel:WORD_1
	v_mul_f32_e32 v3, v135, v3
	v_cvt_f32_f16_sdwa v135, v232 dst_sel:DWORD dst_unused:UNUSED_PAD src0_sel:WORD_1
	v_mul_f32_e32 v94, v94, v3
	v_max_f32_e32 v3, 0x38d1b717, v153
	v_rcp_f32_e32 v3, v3
	v_max_f32_e32 v153, 0x38d1b717, v135
	v_cndmask_b32_e32 v135, v153, v135, vcc
	v_cvt_f32_f16_e32 v153, v229
	v_mul_f32_e32 v3, v135, v3
	v_cvt_f32_f16_e32 v135, v233
	v_mul_f32_e32 v95, v95, v3
	v_max_f32_e32 v3, 0x38d1b717, v153
	v_rcp_f32_e32 v3, v3
	v_max_f32_e32 v153, 0x38d1b717, v135
	v_cndmask_b32_e32 v135, v153, v135, vcc
	v_cvt_f32_f16_sdwa v153, v229 dst_sel:DWORD dst_unused:UNUSED_PAD src0_sel:WORD_1
	v_mul_f32_e32 v3, v135, v3
	v_cvt_f32_f16_sdwa v135, v233 dst_sel:DWORD dst_unused:UNUSED_PAD src0_sel:WORD_1
	v_mul_f32_e32 v96, v96, v3
	v_max_f32_e32 v3, 0x38d1b717, v153
	v_rcp_f32_e32 v3, v3
	v_max_f32_e32 v153, 0x38d1b717, v135
	v_cndmask_b32_e32 v135, v153, v135, vcc
	v_cvt_f32_f16_e32 v153, v234
	v_mul_f32_e32 v3, v135, v3
	v_cvt_f32_f16_e32 v135, v238
	v_mul_f32_e32 v97, v97, v3
	v_max_f32_e32 v3, 0x38d1b717, v153
	v_rcp_f32_e32 v3, v3
	v_max_f32_e32 v153, 0x38d1b717, v135
	v_cndmask_b32_e32 v135, v153, v135, vcc
	v_cvt_f32_f16_sdwa v153, v234 dst_sel:DWORD dst_unused:UNUSED_PAD src0_sel:WORD_1
	v_mul_f32_e32 v3, v135, v3
	v_cvt_f32_f16_sdwa v135, v238 dst_sel:DWORD dst_unused:UNUSED_PAD src0_sel:WORD_1
	v_mul_f32_e32 v90, v90, v3
	v_max_f32_e32 v3, 0x38d1b717, v153
	v_rcp_f32_e32 v3, v3
	v_max_f32_e32 v153, 0x38d1b717, v135
	v_cndmask_b32_e32 v135, v153, v135, vcc
	v_cvt_f32_f16_e32 v153, v235
	v_mul_f32_e32 v3, v135, v3
	v_cvt_f32_f16_e32 v135, v239
	v_mul_f32_e32 v91, v91, v3
	v_max_f32_e32 v3, 0x38d1b717, v153
	v_rcp_f32_e32 v3, v3
	v_max_f32_e32 v153, 0x38d1b717, v135
	v_cndmask_b32_e32 v135, v153, v135, vcc
	v_cvt_f32_f16_sdwa v153, v235 dst_sel:DWORD dst_unused:UNUSED_PAD src0_sel:WORD_1
	v_mul_f32_e32 v3, v135, v3
	v_cvt_f32_f16_sdwa v135, v239 dst_sel:DWORD dst_unused:UNUSED_PAD src0_sel:WORD_1
	v_mul_f32_e32 v92, v92, v3
	v_max_f32_e32 v3, 0x38d1b717, v153
	v_rcp_f32_e32 v3, v3
	v_max_f32_e32 v153, 0x38d1b717, v135
	v_cndmask_b32_e32 v135, v153, v135, vcc
	v_cvt_f32_f16_e32 v153, v236
	v_mul_f32_e32 v3, v135, v3
	v_cvt_f32_f16_e32 v135, v240
	v_mul_f32_e32 v93, v93, v3
	v_max_f32_e32 v3, 0x38d1b717, v153
	v_rcp_f32_e32 v3, v3
	v_max_f32_e32 v153, 0x38d1b717, v135
	v_cndmask_b32_e32 v135, v153, v135, vcc
	v_cvt_f32_f16_sdwa v153, v236 dst_sel:DWORD dst_unused:UNUSED_PAD src0_sel:WORD_1
	v_mul_f32_e32 v3, v135, v3
	v_cvt_f32_f16_sdwa v135, v240 dst_sel:DWORD dst_unused:UNUSED_PAD src0_sel:WORD_1
	v_mul_f32_e32 v86, v86, v3
	v_max_f32_e32 v3, 0x38d1b717, v153
	v_rcp_f32_e32 v3, v3
	v_max_f32_e32 v153, 0x38d1b717, v135
	v_cndmask_b32_e32 v135, v153, v135, vcc
	v_cvt_f32_f16_e32 v153, v237
	v_mul_f32_e32 v3, v135, v3
	v_cvt_f32_f16_e32 v135, v241
	v_mul_f32_e32 v87, v87, v3
	v_max_f32_e32 v3, 0x38d1b717, v153
	v_rcp_f32_e32 v3, v3
	v_cvt_f32_f16_sdwa v155, v237 dst_sel:DWORD dst_unused:UNUSED_PAD src0_sel:WORD_1
	v_max_f32_e32 v153, 0x38d1b717, v135
	v_cndmask_b32_e32 v135, v153, v135, vcc
	v_mul_f32_e32 v3, v135, v3
	v_cvt_f32_f16_sdwa v135, v241 dst_sel:DWORD dst_unused:UNUSED_PAD src0_sel:WORD_1
	v_max_f32_e32 v153, 0x38d1b717, v155
	v_rcp_f32_e32 v153, v153
	v_mul_f32_e32 v88, v88, v3
	v_max_f32_e32 v3, 0x38d1b717, v135
	v_cndmask_b32_e32 v3, v3, v135, vcc
	v_mul_f32_e32 v3, v3, v153
	v_mul_f32_e32 v89, v89, v3
	v_mov_b32_e32 v3, v158
	s_nop 0
	v_mad_i64_i32 v[226:227], s[42:43], v3, s64, v[136:137]
	v_lshl_add_u64 v[234:235], v[226:227], 0, s[16:17]
	v_lshl_add_u64 v[230:231], v[234:235], 0, v[166:167]
	v_lshl_add_u64 v[226:227], v[230:231], 0, s[40:41]
	global_load_dwordx4 v[226:229], v[226:227], off
	v_lshl_add_u64 v[230:231], v[230:231], 0, s[0:1]
	global_load_dwordx4 v[230:233], v[230:231], off
	v_lshl_add_u64 v[238:239], v[234:235], 0, s[0:1]
	v_lshl_add_u64 v[234:235], v[234:235], 0, s[40:41]
	v_lshl_add_u64 v[234:235], v[234:235], 0, v[4:5]
	global_load_dwordx4 v[234:237], v[234:235], off
	v_lshl_add_u64 v[238:239], v[238:239], 0, v[4:5]
	global_load_dwordx4 v[238:241], v[238:239], off
	s_waitcnt vmcnt(4)
	v_cvt_f32_f16_e32 v3, v168
	v_cvt_f32_f16_e32 v135, v176
	v_max_f32_e32 v3, 0x38d1b717, v3
	v_rcp_f32_e32 v3, v3
	v_max_f32_e32 v153, 0x38d1b717, v135
	v_cndmask_b32_e32 v135, v153, v135, vcc
	v_cvt_f32_f16_sdwa v153, v168 dst_sel:DWORD dst_unused:UNUSED_PAD src0_sel:WORD_1
	v_mul_f32_e32 v3, v135, v3
	v_cvt_f32_f16_sdwa v135, v176 dst_sel:DWORD dst_unused:UNUSED_PAD src0_sel:WORD_1
	v_mul_f32_e32 v82, v82, v3
	v_max_f32_e32 v3, 0x38d1b717, v153
	v_rcp_f32_e32 v3, v3
	v_max_f32_e32 v153, 0x38d1b717, v135
	v_cndmask_b32_e32 v135, v153, v135, vcc
	v_cvt_f32_f16_e32 v153, v169
	v_mul_f32_e32 v3, v135, v3
	v_cvt_f32_f16_e32 v135, v177
	v_mul_f32_e32 v83, v83, v3
	v_max_f32_e32 v3, 0x38d1b717, v153
	v_rcp_f32_e32 v3, v3
	v_max_f32_e32 v153, 0x38d1b717, v135
	v_cndmask_b32_e32 v135, v153, v135, vcc
	v_cvt_f32_f16_sdwa v153, v169 dst_sel:DWORD dst_unused:UNUSED_PAD src0_sel:WORD_1
	v_mul_f32_e32 v3, v135, v3
	v_cvt_f32_f16_sdwa v135, v177 dst_sel:DWORD dst_unused:UNUSED_PAD src0_sel:WORD_1
	v_mul_f32_e32 v84, v84, v3
	v_max_f32_e32 v3, 0x38d1b717, v153
	v_rcp_f32_e32 v3, v3
	v_max_f32_e32 v153, 0x38d1b717, v135
	v_cndmask_b32_e32 v135, v153, v135, vcc
	v_cvt_f32_f16_e32 v153, v170
	v_mul_f32_e32 v3, v135, v3
	v_cvt_f32_f16_e32 v135, v178
	v_mul_f32_e32 v85, v85, v3
	v_max_f32_e32 v3, 0x38d1b717, v153
	v_rcp_f32_e32 v3, v3
	v_max_f32_e32 v153, 0x38d1b717, v135
	v_cndmask_b32_e32 v135, v153, v135, vcc
	v_cvt_f32_f16_sdwa v153, v170 dst_sel:DWORD dst_unused:UNUSED_PAD src0_sel:WORD_1
	v_mul_f32_e32 v3, v135, v3
	v_cvt_f32_f16_sdwa v135, v178 dst_sel:DWORD dst_unused:UNUSED_PAD src0_sel:WORD_1
	v_mul_f32_e32 v78, v78, v3
	v_max_f32_e32 v3, 0x38d1b717, v153
	v_rcp_f32_e32 v3, v3
	v_max_f32_e32 v153, 0x38d1b717, v135
	v_cndmask_b32_e32 v135, v153, v135, vcc
	v_cvt_f32_f16_e32 v153, v171
	v_mul_f32_e32 v3, v135, v3
	v_cvt_f32_f16_e32 v135, v179
	v_mul_f32_e32 v79, v79, v3
	v_max_f32_e32 v3, 0x38d1b717, v153
	v_rcp_f32_e32 v3, v3
	v_max_f32_e32 v153, 0x38d1b717, v135
	v_cndmask_b32_e32 v135, v153, v135, vcc
	v_cvt_f32_f16_sdwa v153, v171 dst_sel:DWORD dst_unused:UNUSED_PAD src0_sel:WORD_1
	v_mul_f32_e32 v3, v135, v3
	v_cvt_f32_f16_sdwa v135, v179 dst_sel:DWORD dst_unused:UNUSED_PAD src0_sel:WORD_1
	v_mul_f32_e32 v80, v80, v3
	v_max_f32_e32 v3, 0x38d1b717, v153
	v_rcp_f32_e32 v3, v3
	v_max_f32_e32 v153, 0x38d1b717, v135
	v_cndmask_b32_e32 v135, v153, v135, vcc
	v_cvt_f32_f16_e32 v153, v180
	v_mul_f32_e32 v3, v135, v3
	v_cvt_f32_f16_e32 v135, v184
	v_mul_f32_e32 v81, v81, v3
	v_max_f32_e32 v3, 0x38d1b717, v153
	v_rcp_f32_e32 v3, v3
	v_max_f32_e32 v153, 0x38d1b717, v135
	v_cndmask_b32_e32 v135, v153, v135, vcc
	v_cvt_f32_f16_sdwa v153, v180 dst_sel:DWORD dst_unused:UNUSED_PAD src0_sel:WORD_1
	v_mul_f32_e32 v3, v135, v3
	v_cvt_f32_f16_sdwa v135, v184 dst_sel:DWORD dst_unused:UNUSED_PAD src0_sel:WORD_1
	v_mul_f32_e32 v74, v74, v3
	v_max_f32_e32 v3, 0x38d1b717, v153
	v_rcp_f32_e32 v3, v3
	v_max_f32_e32 v153, 0x38d1b717, v135
	v_cndmask_b32_e32 v135, v153, v135, vcc
	v_cvt_f32_f16_e32 v153, v181
	v_mul_f32_e32 v3, v135, v3
	v_cvt_f32_f16_e32 v135, v185
	v_mul_f32_e32 v75, v75, v3
	v_max_f32_e32 v3, 0x38d1b717, v153
	v_rcp_f32_e32 v3, v3
	v_max_f32_e32 v153, 0x38d1b717, v135
	v_cndmask_b32_e32 v135, v153, v135, vcc
	v_cvt_f32_f16_sdwa v153, v181 dst_sel:DWORD dst_unused:UNUSED_PAD src0_sel:WORD_1
	v_mul_f32_e32 v3, v135, v3
	v_cvt_f32_f16_sdwa v135, v185 dst_sel:DWORD dst_unused:UNUSED_PAD src0_sel:WORD_1
	v_mul_f32_e32 v76, v76, v3
	v_max_f32_e32 v3, 0x38d1b717, v153
	v_rcp_f32_e32 v3, v3
	v_max_f32_e32 v153, 0x38d1b717, v135
	v_cndmask_b32_e32 v135, v153, v135, vcc
	v_cvt_f32_f16_e32 v153, v182
	v_mul_f32_e32 v3, v135, v3
	v_cvt_f32_f16_e32 v135, v186
	v_mul_f32_e32 v77, v77, v3
	v_max_f32_e32 v3, 0x38d1b717, v153
	v_rcp_f32_e32 v3, v3
	v_max_f32_e32 v153, 0x38d1b717, v135
	v_cndmask_b32_e32 v135, v153, v135, vcc
	v_cvt_f32_f16_sdwa v153, v182 dst_sel:DWORD dst_unused:UNUSED_PAD src0_sel:WORD_1
	v_mul_f32_e32 v3, v135, v3
	v_cvt_f32_f16_sdwa v135, v186 dst_sel:DWORD dst_unused:UNUSED_PAD src0_sel:WORD_1
	v_mul_f32_e32 v70, v70, v3
	v_max_f32_e32 v3, 0x38d1b717, v153
	v_rcp_f32_e32 v3, v3
	v_max_f32_e32 v153, 0x38d1b717, v135
	v_cndmask_b32_e32 v135, v153, v135, vcc
	v_cvt_f32_f16_e32 v153, v183
	v_mul_f32_e32 v3, v135, v3
	v_cvt_f32_f16_e32 v135, v187
	v_mul_f32_e32 v71, v71, v3
	v_max_f32_e32 v3, 0x38d1b717, v153
	v_rcp_f32_e32 v3, v3
	v_cvt_f32_f16_sdwa v155, v183 dst_sel:DWORD dst_unused:UNUSED_PAD src0_sel:WORD_1
	v_max_f32_e32 v153, 0x38d1b717, v135
	v_cndmask_b32_e32 v135, v153, v135, vcc
	v_mul_f32_e32 v3, v135, v3
	v_cvt_f32_f16_sdwa v135, v187 dst_sel:DWORD dst_unused:UNUSED_PAD src0_sel:WORD_1
	v_max_f32_e32 v153, 0x38d1b717, v155
	v_rcp_f32_e32 v153, v153
	v_mul_f32_e32 v72, v72, v3
	v_max_f32_e32 v3, 0x38d1b717, v135
	v_cndmask_b32_e32 v3, v3, v135, vcc
	v_mul_f32_e32 v3, v3, v153
	v_mul_f32_e32 v73, v73, v3
	v_mov_b32_e32 v3, v156
	s_nop 0
	v_mad_i64_i32 v[168:169], s[42:43], v3, s64, v[136:137]
	v_lshl_add_u64 v[180:181], v[168:169], 0, s[16:17]
	v_lshl_add_u64 v[176:177], v[180:181], 0, v[166:167]
	v_lshl_add_u64 v[168:169], v[176:177], 0, s[40:41]
	global_load_dwordx4 v[168:171], v[168:169], off
	v_lshl_add_u64 v[176:177], v[176:177], 0, s[0:1]
	global_load_dwordx4 v[176:179], v[176:177], off
	v_lshl_add_u64 v[184:185], v[180:181], 0, s[0:1]
	v_lshl_add_u64 v[180:181], v[180:181], 0, s[40:41]
	v_lshl_add_u64 v[180:181], v[180:181], 0, v[4:5]
	global_load_dwordx4 v[180:183], v[180:181], off
	v_lshl_add_u64 v[184:185], v[184:185], 0, v[4:5]
	global_load_dwordx4 v[184:187], v[184:185], off
	s_waitcnt vmcnt(4)
	v_cvt_f32_f16_e32 v3, v226
	v_cvt_f32_f16_e32 v135, v230
	v_max_f32_e32 v3, 0x38d1b717, v3
	v_rcp_f32_e32 v3, v3
	v_max_f32_e32 v153, 0x38d1b717, v135
	v_cndmask_b32_e32 v135, v153, v135, vcc
	v_cvt_f32_f16_sdwa v153, v226 dst_sel:DWORD dst_unused:UNUSED_PAD src0_sel:WORD_1
	v_mul_f32_e32 v3, v135, v3
	v_cvt_f32_f16_sdwa v135, v230 dst_sel:DWORD dst_unused:UNUSED_PAD src0_sel:WORD_1
	v_mul_f32_e32 v66, v66, v3
	v_max_f32_e32 v3, 0x38d1b717, v153
	v_rcp_f32_e32 v3, v3
	v_max_f32_e32 v153, 0x38d1b717, v135
	v_cndmask_b32_e32 v135, v153, v135, vcc
	v_cvt_f32_f16_e32 v153, v227
	v_mul_f32_e32 v3, v135, v3
	v_cvt_f32_f16_e32 v135, v231
	v_mul_f32_e32 v67, v67, v3
	v_max_f32_e32 v3, 0x38d1b717, v153
	v_rcp_f32_e32 v3, v3
	v_max_f32_e32 v153, 0x38d1b717, v135
	v_cndmask_b32_e32 v135, v153, v135, vcc
	v_cvt_f32_f16_sdwa v153, v227 dst_sel:DWORD dst_unused:UNUSED_PAD src0_sel:WORD_1
	v_mul_f32_e32 v3, v135, v3
	v_cvt_f32_f16_sdwa v135, v231 dst_sel:DWORD dst_unused:UNUSED_PAD src0_sel:WORD_1
	v_mul_f32_e32 v68, v68, v3
	v_max_f32_e32 v3, 0x38d1b717, v153
	v_rcp_f32_e32 v3, v3
	v_max_f32_e32 v153, 0x38d1b717, v135
	v_cndmask_b32_e32 v135, v153, v135, vcc
	v_cvt_f32_f16_e32 v153, v228
	v_mul_f32_e32 v3, v135, v3
	v_cvt_f32_f16_e32 v135, v232
	v_mul_f32_e32 v69, v69, v3
	v_max_f32_e32 v3, 0x38d1b717, v153
	v_rcp_f32_e32 v3, v3
	v_max_f32_e32 v153, 0x38d1b717, v135
	v_cndmask_b32_e32 v135, v153, v135, vcc
	v_cvt_f32_f16_sdwa v153, v228 dst_sel:DWORD dst_unused:UNUSED_PAD src0_sel:WORD_1
	v_mul_f32_e32 v3, v135, v3
	v_cvt_f32_f16_sdwa v135, v232 dst_sel:DWORD dst_unused:UNUSED_PAD src0_sel:WORD_1
	v_mul_f32_e32 v62, v62, v3
	v_max_f32_e32 v3, 0x38d1b717, v153
	v_rcp_f32_e32 v3, v3
	v_max_f32_e32 v153, 0x38d1b717, v135
	v_cndmask_b32_e32 v135, v153, v135, vcc
	v_cvt_f32_f16_e32 v153, v229
	v_mul_f32_e32 v3, v135, v3
	v_cvt_f32_f16_e32 v135, v233
	v_mul_f32_e32 v63, v63, v3
	v_max_f32_e32 v3, 0x38d1b717, v153
	v_rcp_f32_e32 v3, v3
	v_max_f32_e32 v153, 0x38d1b717, v135
	v_cndmask_b32_e32 v135, v153, v135, vcc
	v_cvt_f32_f16_sdwa v153, v229 dst_sel:DWORD dst_unused:UNUSED_PAD src0_sel:WORD_1
	v_mul_f32_e32 v3, v135, v3
	v_cvt_f32_f16_sdwa v135, v233 dst_sel:DWORD dst_unused:UNUSED_PAD src0_sel:WORD_1
	v_mul_f32_e32 v64, v64, v3
	v_max_f32_e32 v3, 0x38d1b717, v153
	v_rcp_f32_e32 v3, v3
	v_max_f32_e32 v153, 0x38d1b717, v135
	v_cndmask_b32_e32 v135, v153, v135, vcc
	v_cvt_f32_f16_e32 v153, v234
	v_mul_f32_e32 v3, v135, v3
	v_cvt_f32_f16_e32 v135, v238
	v_mul_f32_e32 v65, v65, v3
	v_max_f32_e32 v3, 0x38d1b717, v153
	v_rcp_f32_e32 v3, v3
	v_max_f32_e32 v153, 0x38d1b717, v135
	v_cndmask_b32_e32 v135, v153, v135, vcc
	v_cvt_f32_f16_sdwa v153, v234 dst_sel:DWORD dst_unused:UNUSED_PAD src0_sel:WORD_1
	v_mul_f32_e32 v3, v135, v3
	v_cvt_f32_f16_sdwa v135, v238 dst_sel:DWORD dst_unused:UNUSED_PAD src0_sel:WORD_1
	v_mul_f32_e32 v58, v58, v3
	v_max_f32_e32 v3, 0x38d1b717, v153
	v_rcp_f32_e32 v3, v3
	v_max_f32_e32 v153, 0x38d1b717, v135
	v_cndmask_b32_e32 v135, v153, v135, vcc
	v_cvt_f32_f16_e32 v153, v235
	v_mul_f32_e32 v3, v135, v3
	v_cvt_f32_f16_e32 v135, v239
	v_mul_f32_e32 v59, v59, v3
	v_max_f32_e32 v3, 0x38d1b717, v153
	v_rcp_f32_e32 v3, v3
	v_max_f32_e32 v153, 0x38d1b717, v135
	v_cndmask_b32_e32 v135, v153, v135, vcc
	v_cvt_f32_f16_sdwa v153, v235 dst_sel:DWORD dst_unused:UNUSED_PAD src0_sel:WORD_1
	v_mul_f32_e32 v3, v135, v3
	v_cvt_f32_f16_sdwa v135, v239 dst_sel:DWORD dst_unused:UNUSED_PAD src0_sel:WORD_1
	v_mul_f32_e32 v60, v60, v3
	v_max_f32_e32 v3, 0x38d1b717, v153
	v_rcp_f32_e32 v3, v3
	v_max_f32_e32 v153, 0x38d1b717, v135
	v_cndmask_b32_e32 v135, v153, v135, vcc
	v_cvt_f32_f16_e32 v153, v236
	v_mul_f32_e32 v3, v135, v3
	v_cvt_f32_f16_e32 v135, v240
	v_mul_f32_e32 v61, v61, v3
	v_max_f32_e32 v3, 0x38d1b717, v153
	v_rcp_f32_e32 v3, v3
	v_max_f32_e32 v153, 0x38d1b717, v135
	v_cndmask_b32_e32 v135, v153, v135, vcc
	v_cvt_f32_f16_sdwa v153, v236 dst_sel:DWORD dst_unused:UNUSED_PAD src0_sel:WORD_1
	v_mul_f32_e32 v3, v135, v3
	v_cvt_f32_f16_sdwa v135, v240 dst_sel:DWORD dst_unused:UNUSED_PAD src0_sel:WORD_1
	v_mul_f32_e32 v54, v54, v3
	v_max_f32_e32 v3, 0x38d1b717, v153
	v_rcp_f32_e32 v3, v3
	v_max_f32_e32 v153, 0x38d1b717, v135
	v_cndmask_b32_e32 v135, v153, v135, vcc
	v_cvt_f32_f16_e32 v153, v237
	v_mul_f32_e32 v3, v135, v3
	v_cvt_f32_f16_e32 v135, v241
	v_mul_f32_e32 v55, v55, v3
	v_max_f32_e32 v3, 0x38d1b717, v153
	v_rcp_f32_e32 v3, v3
	v_cvt_f32_f16_sdwa v155, v237 dst_sel:DWORD dst_unused:UNUSED_PAD src0_sel:WORD_1
	v_max_f32_e32 v153, 0x38d1b717, v135
	v_cndmask_b32_e32 v135, v153, v135, vcc
	v_mul_f32_e32 v3, v135, v3
	v_cvt_f32_f16_sdwa v135, v241 dst_sel:DWORD dst_unused:UNUSED_PAD src0_sel:WORD_1
	v_max_f32_e32 v153, 0x38d1b717, v155
	v_rcp_f32_e32 v153, v153
	v_mul_f32_e32 v56, v56, v3
	v_max_f32_e32 v3, 0x38d1b717, v135
	v_cndmask_b32_e32 v3, v3, v135, vcc
	v_mul_f32_e32 v3, v3, v153
	v_mul_f32_e32 v57, v57, v3
	v_mov_b32_e32 v3, v154
	s_nop 0
	v_mad_i64_i32 v[226:227], s[42:43], v3, s64, v[136:137]
	v_lshl_add_u64 v[234:235], v[226:227], 0, s[16:17]
	v_lshl_add_u64 v[230:231], v[234:235], 0, v[166:167]
	v_lshl_add_u64 v[226:227], v[230:231], 0, s[40:41]
	global_load_dwordx4 v[226:229], v[226:227], off
	v_lshl_add_u64 v[230:231], v[230:231], 0, s[0:1]
	global_load_dwordx4 v[230:233], v[230:231], off
	v_lshl_add_u64 v[238:239], v[234:235], 0, s[0:1]
	v_lshl_add_u64 v[234:235], v[234:235], 0, s[40:41]
	v_lshl_add_u64 v[234:235], v[234:235], 0, v[4:5]
	global_load_dwordx4 v[234:237], v[234:235], off
	v_lshl_add_u64 v[238:239], v[238:239], 0, v[4:5]
	global_load_dwordx4 v[238:241], v[238:239], off
	s_waitcnt vmcnt(4)
	v_cvt_f32_f16_e32 v3, v168
	v_cvt_f32_f16_e32 v135, v176
	v_max_f32_e32 v3, 0x38d1b717, v3
	v_rcp_f32_e32 v3, v3
	v_max_f32_e32 v153, 0x38d1b717, v135
	v_cndmask_b32_e32 v135, v153, v135, vcc
	v_cvt_f32_f16_sdwa v153, v168 dst_sel:DWORD dst_unused:UNUSED_PAD src0_sel:WORD_1
	v_mul_f32_e32 v3, v135, v3
	v_cvt_f32_f16_sdwa v135, v176 dst_sel:DWORD dst_unused:UNUSED_PAD src0_sel:WORD_1
	v_mul_f32_e32 v50, v50, v3
	v_max_f32_e32 v3, 0x38d1b717, v153
	v_rcp_f32_e32 v3, v3
	v_max_f32_e32 v153, 0x38d1b717, v135
	v_cndmask_b32_e32 v135, v153, v135, vcc
	v_cvt_f32_f16_e32 v153, v169
	v_mul_f32_e32 v3, v135, v3
	v_cvt_f32_f16_e32 v135, v177
	v_mul_f32_e32 v51, v51, v3
	v_max_f32_e32 v3, 0x38d1b717, v153
	v_rcp_f32_e32 v3, v3
	v_max_f32_e32 v153, 0x38d1b717, v135
	v_cndmask_b32_e32 v135, v153, v135, vcc
	v_cvt_f32_f16_sdwa v153, v169 dst_sel:DWORD dst_unused:UNUSED_PAD src0_sel:WORD_1
	v_mul_f32_e32 v3, v135, v3
	v_cvt_f32_f16_sdwa v135, v177 dst_sel:DWORD dst_unused:UNUSED_PAD src0_sel:WORD_1
	v_mul_f32_e32 v52, v52, v3
	v_max_f32_e32 v3, 0x38d1b717, v153
	v_rcp_f32_e32 v3, v3
	v_max_f32_e32 v153, 0x38d1b717, v135
	v_cndmask_b32_e32 v135, v153, v135, vcc
	v_cvt_f32_f16_e32 v153, v170
	v_mul_f32_e32 v3, v135, v3
	v_cvt_f32_f16_e32 v135, v178
	v_mul_f32_e32 v53, v53, v3
	v_max_f32_e32 v3, 0x38d1b717, v153
	v_rcp_f32_e32 v3, v3
	v_max_f32_e32 v153, 0x38d1b717, v135
	v_cndmask_b32_e32 v135, v153, v135, vcc
	v_cvt_f32_f16_sdwa v153, v170 dst_sel:DWORD dst_unused:UNUSED_PAD src0_sel:WORD_1
	v_mul_f32_e32 v3, v135, v3
	v_cvt_f32_f16_sdwa v135, v178 dst_sel:DWORD dst_unused:UNUSED_PAD src0_sel:WORD_1
	v_mul_f32_e32 v46, v46, v3
	v_max_f32_e32 v3, 0x38d1b717, v153
	v_rcp_f32_e32 v3, v3
	v_max_f32_e32 v153, 0x38d1b717, v135
	v_cndmask_b32_e32 v135, v153, v135, vcc
	v_cvt_f32_f16_e32 v153, v171
	v_mul_f32_e32 v3, v135, v3
	v_cvt_f32_f16_e32 v135, v179
	v_mul_f32_e32 v47, v47, v3
	v_max_f32_e32 v3, 0x38d1b717, v153
	v_rcp_f32_e32 v3, v3
	v_max_f32_e32 v153, 0x38d1b717, v135
	v_cndmask_b32_e32 v135, v153, v135, vcc
	v_cvt_f32_f16_sdwa v153, v171 dst_sel:DWORD dst_unused:UNUSED_PAD src0_sel:WORD_1
	v_mul_f32_e32 v3, v135, v3
	v_cvt_f32_f16_sdwa v135, v179 dst_sel:DWORD dst_unused:UNUSED_PAD src0_sel:WORD_1
	v_mul_f32_e32 v48, v48, v3
	v_max_f32_e32 v3, 0x38d1b717, v153
	v_rcp_f32_e32 v3, v3
	v_max_f32_e32 v153, 0x38d1b717, v135
	v_cndmask_b32_e32 v135, v153, v135, vcc
	v_cvt_f32_f16_e32 v153, v180
	v_mul_f32_e32 v3, v135, v3
	v_cvt_f32_f16_e32 v135, v184
	v_mul_f32_e32 v49, v49, v3
	v_max_f32_e32 v3, 0x38d1b717, v153
	v_rcp_f32_e32 v3, v3
	v_max_f32_e32 v153, 0x38d1b717, v135
	v_cndmask_b32_e32 v135, v153, v135, vcc
	v_cvt_f32_f16_sdwa v153, v180 dst_sel:DWORD dst_unused:UNUSED_PAD src0_sel:WORD_1
	v_mul_f32_e32 v3, v135, v3
	v_cvt_f32_f16_sdwa v135, v184 dst_sel:DWORD dst_unused:UNUSED_PAD src0_sel:WORD_1
	v_mul_f32_e32 v42, v42, v3
	v_max_f32_e32 v3, 0x38d1b717, v153
	v_rcp_f32_e32 v3, v3
	v_max_f32_e32 v153, 0x38d1b717, v135
	v_cndmask_b32_e32 v135, v153, v135, vcc
	v_cvt_f32_f16_e32 v153, v181
	v_mul_f32_e32 v3, v135, v3
	v_cvt_f32_f16_e32 v135, v185
	v_mul_f32_e32 v43, v43, v3
	v_max_f32_e32 v3, 0x38d1b717, v153
	v_rcp_f32_e32 v3, v3
	v_max_f32_e32 v153, 0x38d1b717, v135
	v_cndmask_b32_e32 v135, v153, v135, vcc
	v_cvt_f32_f16_sdwa v153, v181 dst_sel:DWORD dst_unused:UNUSED_PAD src0_sel:WORD_1
	v_mul_f32_e32 v3, v135, v3
	v_cvt_f32_f16_sdwa v135, v185 dst_sel:DWORD dst_unused:UNUSED_PAD src0_sel:WORD_1
	v_mul_f32_e32 v44, v44, v3
	v_max_f32_e32 v3, 0x38d1b717, v153
	v_rcp_f32_e32 v3, v3
	v_max_f32_e32 v153, 0x38d1b717, v135
	v_cndmask_b32_e32 v135, v153, v135, vcc
	v_cvt_f32_f16_e32 v153, v182
	v_mul_f32_e32 v3, v135, v3
	v_cvt_f32_f16_e32 v135, v186
	v_mul_f32_e32 v45, v45, v3
	v_max_f32_e32 v3, 0x38d1b717, v153
	v_rcp_f32_e32 v3, v3
	v_max_f32_e32 v153, 0x38d1b717, v135
	v_cndmask_b32_e32 v135, v153, v135, vcc
	v_cvt_f32_f16_sdwa v153, v182 dst_sel:DWORD dst_unused:UNUSED_PAD src0_sel:WORD_1
	v_mul_f32_e32 v3, v135, v3
	v_cvt_f32_f16_sdwa v135, v186 dst_sel:DWORD dst_unused:UNUSED_PAD src0_sel:WORD_1
	v_mul_f32_e32 v38, v38, v3
	v_max_f32_e32 v3, 0x38d1b717, v153
	v_rcp_f32_e32 v3, v3
	v_max_f32_e32 v153, 0x38d1b717, v135
	v_cndmask_b32_e32 v135, v153, v135, vcc
	v_cvt_f32_f16_e32 v153, v183
	v_mul_f32_e32 v3, v135, v3
	v_cvt_f32_f16_e32 v135, v187
	v_mul_f32_e32 v39, v39, v3
	v_max_f32_e32 v3, 0x38d1b717, v153
	v_rcp_f32_e32 v3, v3
	v_cvt_f32_f16_sdwa v155, v183 dst_sel:DWORD dst_unused:UNUSED_PAD src0_sel:WORD_1
	v_max_f32_e32 v153, 0x38d1b717, v135
	v_cndmask_b32_e32 v135, v153, v135, vcc
	v_mul_f32_e32 v3, v135, v3
	v_cvt_f32_f16_sdwa v135, v187 dst_sel:DWORD dst_unused:UNUSED_PAD src0_sel:WORD_1
	v_max_f32_e32 v153, 0x38d1b717, v155
	v_rcp_f32_e32 v153, v153
	v_mul_f32_e32 v40, v40, v3
	v_max_f32_e32 v3, 0x38d1b717, v135
	v_cndmask_b32_e32 v3, v3, v135, vcc
	v_mul_f32_e32 v3, v3, v153
	v_mul_f32_e32 v41, v41, v3
	v_mov_b32_e32 v3, v152
	s_nop 0
	v_mad_i64_i32 v[136:137], s[42:43], v3, s64, v[136:137]
	v_lshl_add_u64 v[136:137], v[136:137], 0, s[16:17]
	v_lshl_add_u64 v[170:171], v[136:137], 0, v[166:167]
	v_lshl_add_u64 v[166:167], v[170:171], 0, s[40:41]
	global_load_dwordx4 v[166:169], v[166:167], off
	v_lshl_add_u64 v[170:171], v[170:171], 0, s[0:1]
	global_load_dwordx4 v[176:179], v[170:171], off
	v_lshl_add_u64 v[170:171], v[136:137], 0, s[0:1]
	v_lshl_add_u64 v[136:137], v[136:137], 0, s[40:41]
	v_lshl_add_u64 v[136:137], v[136:137], 0, v[4:5]
	global_load_dwordx4 v[180:183], v[136:137], off
	v_lshl_add_u64 v[4:5], v[170:171], 0, v[4:5]
	global_load_dwordx4 v[184:187], v[4:5], off
	s_waitcnt vmcnt(4)
	v_cvt_f32_f16_e32 v3, v226
	v_cvt_f32_f16_e32 v135, v230
	v_max_f32_e32 v3, 0x38d1b717, v3
	v_rcp_f32_e32 v3, v3
	v_max_f32_e32 v153, 0x38d1b717, v135
	v_cndmask_b32_e32 v135, v153, v135, vcc
	v_cvt_f32_f16_sdwa v153, v226 dst_sel:DWORD dst_unused:UNUSED_PAD src0_sel:WORD_1
	v_mul_f32_e32 v3, v135, v3
	v_cvt_f32_f16_sdwa v135, v230 dst_sel:DWORD dst_unused:UNUSED_PAD src0_sel:WORD_1
	v_mul_f32_e32 v34, v34, v3
	v_max_f32_e32 v3, 0x38d1b717, v153
	v_rcp_f32_e32 v3, v3
	v_max_f32_e32 v153, 0x38d1b717, v135
	v_cndmask_b32_e32 v135, v153, v135, vcc
	v_cvt_f32_f16_e32 v153, v227
	v_mul_f32_e32 v3, v135, v3
	v_cvt_f32_f16_e32 v135, v231
	v_mul_f32_e32 v35, v35, v3
	v_max_f32_e32 v3, 0x38d1b717, v153
	v_rcp_f32_e32 v3, v3
	v_max_f32_e32 v153, 0x38d1b717, v135
	v_cndmask_b32_e32 v135, v153, v135, vcc
	v_cvt_f32_f16_sdwa v153, v227 dst_sel:DWORD dst_unused:UNUSED_PAD src0_sel:WORD_1
	v_mul_f32_e32 v3, v135, v3
	v_cvt_f32_f16_sdwa v135, v231 dst_sel:DWORD dst_unused:UNUSED_PAD src0_sel:WORD_1
	v_mul_f32_e32 v36, v36, v3
	v_max_f32_e32 v3, 0x38d1b717, v153
	v_rcp_f32_e32 v3, v3
	v_max_f32_e32 v153, 0x38d1b717, v135
	v_cndmask_b32_e32 v135, v153, v135, vcc
	v_cvt_f32_f16_e32 v153, v228
	v_mul_f32_e32 v3, v135, v3
	v_cvt_f32_f16_e32 v135, v232
	v_mul_f32_e32 v37, v37, v3
	v_max_f32_e32 v3, 0x38d1b717, v153
	v_rcp_f32_e32 v3, v3
	v_max_f32_e32 v153, 0x38d1b717, v135
	v_cndmask_b32_e32 v135, v153, v135, vcc
	v_cvt_f32_f16_sdwa v153, v228 dst_sel:DWORD dst_unused:UNUSED_PAD src0_sel:WORD_1
	v_mul_f32_e32 v3, v135, v3
	v_cvt_f32_f16_sdwa v135, v232 dst_sel:DWORD dst_unused:UNUSED_PAD src0_sel:WORD_1
	v_mul_f32_e32 v30, v30, v3
	v_max_f32_e32 v3, 0x38d1b717, v153
	v_rcp_f32_e32 v3, v3
	v_max_f32_e32 v153, 0x38d1b717, v135
	v_cndmask_b32_e32 v135, v153, v135, vcc
	v_cvt_f32_f16_e32 v153, v229
	v_mul_f32_e32 v3, v135, v3
	v_cvt_f32_f16_e32 v135, v233
	v_mul_f32_e32 v31, v31, v3
	v_max_f32_e32 v3, 0x38d1b717, v153
	v_rcp_f32_e32 v3, v3
	v_max_f32_e32 v153, 0x38d1b717, v135
	v_cndmask_b32_e32 v135, v153, v135, vcc
	v_cvt_f32_f16_sdwa v153, v229 dst_sel:DWORD dst_unused:UNUSED_PAD src0_sel:WORD_1
	v_mul_f32_e32 v3, v135, v3
	v_cvt_f32_f16_sdwa v135, v233 dst_sel:DWORD dst_unused:UNUSED_PAD src0_sel:WORD_1
	v_mul_f32_e32 v32, v32, v3
	v_max_f32_e32 v3, 0x38d1b717, v153
	v_rcp_f32_e32 v3, v3
	v_max_f32_e32 v153, 0x38d1b717, v135
	v_cndmask_b32_e32 v135, v153, v135, vcc
	v_cvt_f32_f16_e32 v153, v234
	v_mul_f32_e32 v3, v135, v3
	v_cvt_f32_f16_e32 v135, v238
	v_mul_f32_e32 v33, v33, v3
	v_max_f32_e32 v3, 0x38d1b717, v153
	v_rcp_f32_e32 v3, v3
	v_max_f32_e32 v153, 0x38d1b717, v135
	v_cndmask_b32_e32 v135, v153, v135, vcc
	v_cvt_f32_f16_sdwa v153, v234 dst_sel:DWORD dst_unused:UNUSED_PAD src0_sel:WORD_1
	v_mul_f32_e32 v3, v135, v3
	v_cvt_f32_f16_sdwa v135, v238 dst_sel:DWORD dst_unused:UNUSED_PAD src0_sel:WORD_1
	v_mul_f32_e32 v26, v26, v3
	v_max_f32_e32 v3, 0x38d1b717, v153
	v_rcp_f32_e32 v3, v3
	v_max_f32_e32 v153, 0x38d1b717, v135
	v_cndmask_b32_e32 v135, v153, v135, vcc
	v_cvt_f32_f16_e32 v153, v235
	v_mul_f32_e32 v3, v135, v3
	v_cvt_f32_f16_e32 v135, v239
	v_mul_f32_e32 v27, v27, v3
	v_max_f32_e32 v3, 0x38d1b717, v153
	v_rcp_f32_e32 v3, v3
	v_max_f32_e32 v153, 0x38d1b717, v135
	v_cndmask_b32_e32 v135, v153, v135, vcc
	v_cvt_f32_f16_sdwa v153, v235 dst_sel:DWORD dst_unused:UNUSED_PAD src0_sel:WORD_1
	v_mul_f32_e32 v3, v135, v3
	v_cvt_f32_f16_sdwa v135, v239 dst_sel:DWORD dst_unused:UNUSED_PAD src0_sel:WORD_1
	v_mul_f32_e32 v28, v28, v3
	v_max_f32_e32 v3, 0x38d1b717, v153
	v_rcp_f32_e32 v3, v3
	v_max_f32_e32 v153, 0x38d1b717, v135
	v_cndmask_b32_e32 v135, v153, v135, vcc
	v_cvt_f32_f16_e32 v153, v236
	v_mul_f32_e32 v3, v135, v3
	v_cvt_f32_f16_e32 v135, v240
	v_mul_f32_e32 v29, v29, v3
	v_max_f32_e32 v3, 0x38d1b717, v153
	v_rcp_f32_e32 v3, v3
	v_max_f32_e32 v153, 0x38d1b717, v135
	v_cndmask_b32_e32 v135, v153, v135, vcc
	v_cvt_f32_f16_sdwa v153, v236 dst_sel:DWORD dst_unused:UNUSED_PAD src0_sel:WORD_1
	v_mul_f32_e32 v3, v135, v3
	v_cvt_f32_f16_sdwa v135, v240 dst_sel:DWORD dst_unused:UNUSED_PAD src0_sel:WORD_1
	v_mul_f32_e32 v22, v22, v3
	v_max_f32_e32 v3, 0x38d1b717, v153
	v_rcp_f32_e32 v3, v3
	v_max_f32_e32 v153, 0x38d1b717, v135
	v_cndmask_b32_e32 v135, v153, v135, vcc
	v_cvt_f32_f16_e32 v153, v237
	v_mul_f32_e32 v3, v135, v3
	v_cvt_f32_f16_e32 v135, v241
	v_mul_f32_e32 v23, v23, v3
	v_max_f32_e32 v3, 0x38d1b717, v153
	v_rcp_f32_e32 v3, v3
	v_cvt_f32_f16_sdwa v155, v237 dst_sel:DWORD dst_unused:UNUSED_PAD src0_sel:WORD_1
	v_max_f32_e32 v153, 0x38d1b717, v135
	v_cndmask_b32_e32 v135, v153, v135, vcc
	v_mul_f32_e32 v3, v135, v3
	v_cvt_f32_f16_sdwa v135, v241 dst_sel:DWORD dst_unused:UNUSED_PAD src0_sel:WORD_1
	v_max_f32_e32 v153, 0x38d1b717, v155
	v_rcp_f32_e32 v153, v153
	v_mul_f32_e32 v24, v24, v3
	v_max_f32_e32 v3, 0x38d1b717, v135
	v_cndmask_b32_e32 v3, v3, v135, vcc
	v_mul_f32_e32 v3, v3, v153
	v_mul_f32_e32 v25, v25, v3
	s_waitcnt vmcnt(0)
	v_cvt_f32_f16_e32 v3, v166
	v_cvt_f32_f16_e32 v4, v176
	v_max_f32_e32 v3, 0x38d1b717, v3
	v_rcp_f32_e32 v3, v3
	v_max_f32_e32 v5, 0x38d1b717, v4
	v_cndmask_b32_e32 v4, v5, v4, vcc
	v_cvt_f32_f16_sdwa v5, v166 dst_sel:DWORD dst_unused:UNUSED_PAD src0_sel:WORD_1
	v_mul_f32_e32 v3, v4, v3
	v_cvt_f32_f16_sdwa v4, v176 dst_sel:DWORD dst_unused:UNUSED_PAD src0_sel:WORD_1
	v_mul_f32_e32 v18, v18, v3
	v_max_f32_e32 v3, 0x38d1b717, v5
	v_rcp_f32_e32 v3, v3
	v_max_f32_e32 v5, 0x38d1b717, v4
	v_cndmask_b32_e32 v4, v5, v4, vcc
	v_cvt_f32_f16_e32 v5, v167
	v_mul_f32_e32 v3, v4, v3
	v_cvt_f32_f16_e32 v4, v177
	v_mul_f32_e32 v19, v19, v3
	v_max_f32_e32 v3, 0x38d1b717, v5
	v_rcp_f32_e32 v3, v3
	v_max_f32_e32 v5, 0x38d1b717, v4
	v_cndmask_b32_e32 v4, v5, v4, vcc
	v_cvt_f32_f16_sdwa v5, v167 dst_sel:DWORD dst_unused:UNUSED_PAD src0_sel:WORD_1
	v_mul_f32_e32 v3, v4, v3
	v_cvt_f32_f16_sdwa v4, v177 dst_sel:DWORD dst_unused:UNUSED_PAD src0_sel:WORD_1
	v_mul_f32_e32 v20, v20, v3
	v_max_f32_e32 v3, 0x38d1b717, v5
	v_rcp_f32_e32 v3, v3
	v_max_f32_e32 v5, 0x38d1b717, v4
	v_cndmask_b32_e32 v4, v5, v4, vcc
	v_cvt_f32_f16_e32 v5, v168
	v_mul_f32_e32 v3, v4, v3
	v_cvt_f32_f16_e32 v4, v178
	v_mul_f32_e32 v21, v21, v3
	v_max_f32_e32 v3, 0x38d1b717, v5
	v_rcp_f32_e32 v3, v3
	v_max_f32_e32 v5, 0x38d1b717, v4
	v_cndmask_b32_e32 v4, v5, v4, vcc
	v_cvt_f32_f16_sdwa v5, v168 dst_sel:DWORD dst_unused:UNUSED_PAD src0_sel:WORD_1
	v_mul_f32_e32 v3, v4, v3
	v_cvt_f32_f16_sdwa v4, v178 dst_sel:DWORD dst_unused:UNUSED_PAD src0_sel:WORD_1
	v_mul_f32_e32 v14, v14, v3
	v_max_f32_e32 v3, 0x38d1b717, v5
	v_rcp_f32_e32 v3, v3
	v_max_f32_e32 v5, 0x38d1b717, v4
	v_cndmask_b32_e32 v4, v5, v4, vcc
	v_cvt_f32_f16_e32 v5, v169
	v_mul_f32_e32 v3, v4, v3
	v_cvt_f32_f16_e32 v4, v179
	v_mul_f32_e32 v15, v15, v3
	v_max_f32_e32 v3, 0x38d1b717, v5
	v_rcp_f32_e32 v3, v3
	v_max_f32_e32 v5, 0x38d1b717, v4
	v_cndmask_b32_e32 v4, v5, v4, vcc
	v_cvt_f32_f16_sdwa v5, v169 dst_sel:DWORD dst_unused:UNUSED_PAD src0_sel:WORD_1
	v_mul_f32_e32 v3, v4, v3
	v_cvt_f32_f16_sdwa v4, v179 dst_sel:DWORD dst_unused:UNUSED_PAD src0_sel:WORD_1
	v_mul_f32_e32 v16, v16, v3
	v_max_f32_e32 v3, 0x38d1b717, v5
	v_rcp_f32_e32 v3, v3
	v_max_f32_e32 v5, 0x38d1b717, v4
	v_cndmask_b32_e32 v4, v5, v4, vcc
	v_cvt_f32_f16_e32 v5, v180
	v_mul_f32_e32 v3, v4, v3
	v_cvt_f32_f16_e32 v4, v184
	v_mul_f32_e32 v17, v17, v3
	v_max_f32_e32 v3, 0x38d1b717, v5
	v_rcp_f32_e32 v3, v3
	v_max_f32_e32 v5, 0x38d1b717, v4
	v_cndmask_b32_e32 v4, v5, v4, vcc
	v_cvt_f32_f16_sdwa v5, v180 dst_sel:DWORD dst_unused:UNUSED_PAD src0_sel:WORD_1
	v_mul_f32_e32 v3, v4, v3
	v_cvt_f32_f16_sdwa v4, v184 dst_sel:DWORD dst_unused:UNUSED_PAD src0_sel:WORD_1
	v_mul_f32_e32 v10, v10, v3
	v_max_f32_e32 v3, 0x38d1b717, v5
	v_rcp_f32_e32 v3, v3
	v_max_f32_e32 v5, 0x38d1b717, v4
	v_cndmask_b32_e32 v4, v5, v4, vcc
	v_cvt_f32_f16_e32 v5, v181
	v_mul_f32_e32 v3, v4, v3
	v_cvt_f32_f16_e32 v4, v185
	v_mul_f32_e32 v11, v11, v3
	v_max_f32_e32 v3, 0x38d1b717, v5
	v_rcp_f32_e32 v3, v3
	v_max_f32_e32 v5, 0x38d1b717, v4
	v_cndmask_b32_e32 v4, v5, v4, vcc
	v_cvt_f32_f16_sdwa v5, v181 dst_sel:DWORD dst_unused:UNUSED_PAD src0_sel:WORD_1
	v_mul_f32_e32 v3, v4, v3
	v_cvt_f32_f16_sdwa v4, v185 dst_sel:DWORD dst_unused:UNUSED_PAD src0_sel:WORD_1
	v_mul_f32_e32 v12, v12, v3
	v_max_f32_e32 v3, 0x38d1b717, v5
	v_rcp_f32_e32 v3, v3
	v_max_f32_e32 v5, 0x38d1b717, v4
	v_cndmask_b32_e32 v4, v5, v4, vcc
	v_cvt_f32_f16_e32 v5, v182
	v_mul_f32_e32 v3, v4, v3
	v_cvt_f32_f16_e32 v4, v186
	v_mul_f32_e32 v13, v13, v3
	v_max_f32_e32 v3, 0x38d1b717, v5
	v_rcp_f32_e32 v3, v3
	v_max_f32_e32 v5, 0x38d1b717, v4
	v_cndmask_b32_e32 v4, v5, v4, vcc
	v_cvt_f32_f16_sdwa v5, v182 dst_sel:DWORD dst_unused:UNUSED_PAD src0_sel:WORD_1
	v_mul_f32_e32 v3, v4, v3
	v_cvt_f32_f16_sdwa v4, v186 dst_sel:DWORD dst_unused:UNUSED_PAD src0_sel:WORD_1
	v_mul_f32_e32 v6, v6, v3
	v_max_f32_e32 v3, 0x38d1b717, v5
	v_rcp_f32_e32 v3, v3
	v_max_f32_e32 v5, 0x38d1b717, v4
	v_cndmask_b32_e32 v4, v5, v4, vcc
	v_cvt_f32_f16_e32 v5, v183
	v_mul_f32_e32 v3, v4, v3
	v_cvt_f32_f16_e32 v4, v187
	v_mul_f32_e32 v7, v7, v3
	v_max_f32_e32 v3, 0x38d1b717, v5
	v_rcp_f32_e32 v3, v3
	v_cvt_f32_f16_sdwa v135, v183 dst_sel:DWORD dst_unused:UNUSED_PAD src0_sel:WORD_1
	v_max_f32_e32 v5, 0x38d1b717, v4
	v_cndmask_b32_e32 v4, v5, v4, vcc
	v_mul_f32_e32 v3, v4, v3
	v_cvt_f32_f16_sdwa v4, v187 dst_sel:DWORD dst_unused:UNUSED_PAD src0_sel:WORD_1
	v_max_f32_e32 v5, 0x38d1b717, v135
	v_rcp_f32_e32 v5, v5
	v_mul_f32_e32 v8, v8, v3
	v_max_f32_e32 v3, 0x38d1b717, v4
	v_cndmask_b32_e32 v3, v3, v4, vcc
	v_mul_f32_e32 v3, v3, v5
	v_mul_f32_e32 v9, v9, v3
	s_branch .LBB0_964

.LBB0_977:
	v_mov_b32_e32 v238, s6
	v_min_u32_e32 v238, 2, v238
	v_lshlrev_b32_e32 v238, 11, v238
	v_add_u32_e32 v238, 0x1800, v238
	v_mov_b64_e32 v[226:227], s[8:9]
	v_lshlrev_b64 v[228:229], 1, v[148:149]
	v_lshlrev_b64 v[230:231], 1, v[150:151]
	v_add_co_u32_e32 v228, vcc, v228, v238
	v_addc_co_u32_e32 v229, vcc, 0, v229, vcc
	v_add_co_u32_e32 v230, vcc, v230, v238
	v_addc_co_u32_e32 v231, vcc, 0, v231, vcc
	v_mad_i64_i32 v[232:233], s[34:35], v134, s64, v[226:227]
	v_lshl_add_u64 v[234:235], v[232:233], 0, v[228:229]
	v_lshl_add_u64 v[236:237], v[232:233], 0, v[230:231]
	global_load_dword v213, v[234:235], off
	global_load_dword v213, v[236:237], off
	v_mad_i64_i32 v[232:233], s[34:35], v164, s64, v[226:227]
	v_lshl_add_u64 v[234:235], v[232:233], 0, v[228:229]
	v_lshl_add_u64 v[236:237], v[232:233], 0, v[230:231]
	global_load_dword v213, v[234:235], off
	global_load_dword v213, v[236:237], off
	v_mad_i64_i32 v[232:233], s[34:35], v162, s64, v[226:227]
	v_lshl_add_u64 v[234:235], v[232:233], 0, v[228:229]
	v_lshl_add_u64 v[236:237], v[232:233], 0, v[230:231]
	global_load_dword v213, v[234:235], off
	global_load_dword v213, v[236:237], off
	v_mad_i64_i32 v[232:233], s[34:35], v160, s64, v[226:227]
	v_lshl_add_u64 v[234:235], v[232:233], 0, v[228:229]
	v_lshl_add_u64 v[236:237], v[232:233], 0, v[230:231]
	global_load_dword v213, v[234:235], off
	global_load_dword v213, v[236:237], off
	v_mad_i64_i32 v[232:233], s[34:35], v158, s64, v[226:227]
	v_lshl_add_u64 v[234:235], v[232:233], 0, v[228:229]
	v_lshl_add_u64 v[236:237], v[232:233], 0, v[230:231]
	global_load_dword v213, v[234:235], off
	global_load_dword v213, v[236:237], off
	v_mad_i64_i32 v[232:233], s[34:35], v156, s64, v[226:227]
	v_lshl_add_u64 v[234:235], v[232:233], 0, v[228:229]
	v_lshl_add_u64 v[236:237], v[232:233], 0, v[230:231]
	global_load_dword v213, v[234:235], off
	global_load_dword v213, v[236:237], off
	v_mad_i64_i32 v[232:233], s[34:35], v154, s64, v[226:227]
	v_lshl_add_u64 v[234:235], v[232:233], 0, v[228:229]
	v_lshl_add_u64 v[236:237], v[232:233], 0, v[230:231]
	global_load_dword v213, v[234:235], off
	global_load_dword v213, v[236:237], off
	v_mad_i64_i32 v[232:233], s[34:35], v152, s64, v[226:227]
	v_lshl_add_u64 v[234:235], v[232:233], 0, v[228:229]
	v_lshl_add_u64 v[236:237], v[232:233], 0, v[230:231]
	global_load_dword v213, v[234:235], off
	global_load_dword v213, v[236:237], off
	s_cmp_lt_i32 s6, 0
	s_cselect_b64 s[36:37], -1, 0
	v_ashrrev_i32_e32 v135, 31, v134
	s_cmp_eq_u32 s6, 0
	v_lshlrev_b64 v[168:169], 11, v[134:135]
	v_mov_b64_e32 v[4:5], s[8:9]
	s_cselect_b64 s[4:5], -1, 0
	v_mad_i64_i32 v[166:167], s[34:35], v134, s64, v[4:5]
	s_mov_b64 s[38:39], -1
	s_and_b64 vcc, exec, s[36:37]
	v_lshl_add_u64 v[4:5], s[10:11], 0, v[168:169]
	s_cbranch_vccz .LBB0_979
	v_lshl_add_u64 v[134:135], v[148:149], 1, v[166:167]
	v_add_co_u32_e32 v134, vcc, 0x2000, v134
	v_mov_b32_e32 v176, v131
	s_nop 0
	v_addc_co_u32_e32 v135, vcc, 0, v135, vcc
	global_load_dwordx4 v[134:137], v[134:135], off offset:2048
	v_mov_b32_e32 v177, v132
	v_pk_mov_b32 v[178:179], v[132:133], v[126:127] op_sel:[1,0]
	v_mov_b32_e32 v180, v127
	v_mov_b32_e32 v181, v128
	v_lshl_add_u64 v[170:171], s[10:11], 0, v[168:169]
	s_mov_b64 s[38:39], 0
	s_waitcnt vmcnt(0)
	v_cvt_f32_f16_e32 v3, v134
	v_cvt_f32_f16_sdwa v134, v134 dst_sel:DWORD dst_unused:UNUSED_PAD src0_sel:WORD_1
	v_cvt_f32_f16_e32 v153, v135
	v_cvt_f32_f16_sdwa v155, v135 dst_sel:DWORD dst_unused:UNUSED_PAD src0_sel:WORD_1
	v_cvt_f32_f16_e32 v157, v136
	v_cvt_f32_f16_sdwa v159, v136 dst_sel:DWORD dst_unused:UNUSED_PAD src0_sel:WORD_1
	v_cvt_f32_f16_e32 v161, v137
	v_cvt_f32_f16_sdwa v163, v137 dst_sel:DWORD dst_unused:UNUSED_PAD src0_sel:WORD_1
	v_max_f32_e32 v134, 0x38d1b717, v134
	v_max_f32_e32 v135, 0x38d1b717, v153
	v_max_f32_e32 v136, 0x38d1b717, v155
	v_max_f32_e32 v137, 0x38d1b717, v157
	v_max_f32_e32 v182, 0x38d1b717, v159
	v_max_f32_e32 v183, 0x38d1b717, v161
	v_max_f32_e32 v3, 0x38d1b717, v3
	v_pk_mul_f32 v[134:135], v[176:177], v[134:135]
	v_pk_mul_f32 v[136:137], v[178:179], v[136:137]
	v_pk_mul_f32 v[176:177], v[180:181], v[182:183]
	v_fma_mixlo_f16 v3, v130, v3, 0
	v_cvt_pk_f16_f32 v135, v134, v135
	v_cvt_pk_f16_f32 v136, v136, v137
	v_cvt_pk_f16_f32 v137, v176, v177
	v_max_f32_e32 v153, 0x38d1b717, v163
	v_pack_b32_f16 v134, v3, v135
	v_alignbit_b32 v135, v136, v135, 16
	v_alignbit_b32 v136, v137, v136, 16
	v_lshrrev_b32_e32 v137, 16, v137
	v_fma_mixhi_f16 v137, v129, v153, 0

.LBB0_5355:
	s_cmp_lg_u32 s65, 2
	s_cselect_b64 s[38:39], -1, 0
	s_and_b64 s[38:39], s[38:39], s[34:35]
	s_andn2_b64 vcc, exec, s[38:39]
	s_cbranch_vccnz .LBB0_5351
	v_mov_b32_e32 v3, v134
	v_mov_b64_e32 v[136:137], s[8:9]
	s_and_b64 s[38:39], s[0:1], exec
	v_mad_i64_i32 v[4:5], s[40:41], v3, s62, v[136:137]
	v_lshl_add_u64 v[234:235], v[4:5], 0, s[16:17]
	v_lshlrev_b64 v[166:167], 1, v[148:149]
	s_cselect_b32 s2, 0, 0x800
	v_lshl_add_u64 v[4:5], v[234:235], 0, v[166:167]
	s_cselect_b32 s38, 0x800, s61
	s_mov_b32 s39, s3
	v_lshl_add_u64 v[226:227], v[4:5], 0, s[2:3]
	v_lshl_add_u64 v[4:5], v[4:5], 0, s[38:39]
	global_load_dwordx4 v[226:229], v[226:227], off
	s_nop 0
	global_load_dwordx4 v[230:233], v[4:5], off
	v_lshlrev_b64 v[4:5], 1, v[150:151]
	v_lshl_add_u64 v[236:237], v[234:235], 0, s[2:3]
	v_lshl_add_u64 v[234:235], v[234:235], 0, s[38:39]
	v_lshl_add_u64 v[236:237], v[236:237], 0, v[4:5]
	v_lshl_add_u64 v[238:239], v[234:235], 0, v[4:5]
	global_load_dwordx4 v[234:237], v[236:237], off
	s_nop 0
	global_load_dwordx4 v[238:241], v[238:239], off
	v_mad_i64_i32 v[188:189], s[40:41], v162, s62, v[136:137]
	v_lshl_add_u64 v[188:189], v[188:189], 0, s[16:17]
	v_lshl_add_u64 v[190:191], v[188:189], 0, v[166:167]
	v_lshl_add_u64 v[192:193], v[190:191], 0, s[38:39]
	global_load_dword v213, v[192:193], off
	v_lshl_add_u64 v[190:191], v[190:191], 0, s[2:3]
	global_load_dword v213, v[190:191], off
	v_lshl_add_u64 v[188:189], v[188:189], 0, v[4:5]
	v_lshl_add_u64 v[192:193], v[188:189], 0, s[38:39]
	global_load_dword v213, v[192:193], off
	v_lshl_add_u64 v[188:189], v[188:189], 0, s[2:3]
	global_load_dword v213, v[188:189], off
	v_mad_i64_i32 v[188:189], s[40:41], v160, s62, v[136:137]
	v_lshl_add_u64 v[188:189], v[188:189], 0, s[16:17]
	v_lshl_add_u64 v[190:191], v[188:189], 0, v[166:167]
	v_lshl_add_u64 v[192:193], v[190:191], 0, s[38:39]
	global_load_dword v213, v[192:193], off
	v_lshl_add_u64 v[190:191], v[190:191], 0, s[2:3]
	global_load_dword v213, v[190:191], off
	v_lshl_add_u64 v[188:189], v[188:189], 0, v[4:5]
	v_lshl_add_u64 v[192:193], v[188:189], 0, s[38:39]
	global_load_dword v213, v[192:193], off
	v_lshl_add_u64 v[188:189], v[188:189], 0, s[2:3]
	global_load_dword v213, v[188:189], off
	v_mad_i64_i32 v[188:189], s[40:41], v158, s62, v[136:137]
	v_lshl_add_u64 v[188:189], v[188:189], 0, s[16:17]
	v_lshl_add_u64 v[190:191], v[188:189], 0, v[166:167]
	v_lshl_add_u64 v[192:193], v[190:191], 0, s[38:39]
	global_load_dword v213, v[192:193], off
	v_lshl_add_u64 v[190:191], v[190:191], 0, s[2:3]
	global_load_dword v213, v[190:191], off
	v_lshl_add_u64 v[188:189], v[188:189], 0, v[4:5]
	v_lshl_add_u64 v[192:193], v[188:189], 0, s[38:39]
	global_load_dword v213, v[192:193], off
	v_lshl_add_u64 v[188:189], v[188:189], 0, s[2:3]
	global_load_dword v213, v[188:189], off
	v_mad_i64_i32 v[188:189], s[40:41], v156, s62, v[136:137]
	v_lshl_add_u64 v[188:189], v[188:189], 0, s[16:17]
	v_lshl_add_u64 v[190:191], v[188:189], 0, v[166:167]
	v_lshl_add_u64 v[192:193], v[190:191], 0, s[38:39]
	global_load_dword v213, v[192:193], off
	v_lshl_add_u64 v[190:191], v[190:191], 0, s[2:3]
	global_load_dword v213, v[190:191], off
	v_lshl_add_u64 v[188:189], v[188:189], 0, v[4:5]
	v_lshl_add_u64 v[192:193], v[188:189], 0, s[38:39]
	global_load_dword v213, v[192:193], off
	v_lshl_add_u64 v[188:189], v[188:189], 0, s[2:3]
	global_load_dword v213, v[188:189], off
	v_mad_i64_i32 v[188:189], s[40:41], v154, s62, v[136:137]
	v_lshl_add_u64 v[188:189], v[188:189], 0, s[16:17]
	v_lshl_add_u64 v[190:191], v[188:189], 0, v[166:167]
	v_lshl_add_u64 v[192:193], v[190:191], 0, s[38:39]
	global_load_dword v213, v[192:193], off
	v_lshl_add_u64 v[190:191], v[190:191], 0, s[2:3]
	global_load_dword v213, v[190:191], off
	v_lshl_add_u64 v[188:189], v[188:189], 0, v[4:5]
	v_lshl_add_u64 v[192:193], v[188:189], 0, s[38:39]
	global_load_dword v213, v[192:193], off
	v_lshl_add_u64 v[188:189], v[188:189], 0, s[2:3]
	global_load_dword v213, v[188:189], off
	v_mad_i64_i32 v[188:189], s[40:41], v152, s62, v[136:137]
	v_lshl_add_u64 v[188:189], v[188:189], 0, s[16:17]
	v_lshl_add_u64 v[190:191], v[188:189], 0, v[166:167]
	v_lshl_add_u64 v[192:193], v[190:191], 0, s[38:39]
	global_load_dword v213, v[192:193], off
	v_lshl_add_u64 v[190:191], v[190:191], 0, s[2:3]
	global_load_dword v213, v[190:191], off
	v_lshl_add_u64 v[188:189], v[188:189], 0, v[4:5]
	v_lshl_add_u64 v[192:193], v[188:189], 0, s[38:39]
	global_load_dword v213, v[192:193], off
	v_lshl_add_u64 v[188:189], v[188:189], 0, s[2:3]
	global_load_dword v213, v[188:189], off
	v_mov_b32_e32 v3, v164
	s_nop 0
	v_mad_i64_i32 v[168:169], s[40:41], v3, s62, v[136:137]
	v_lshl_add_u64 v[180:181], v[168:169], 0, s[16:17]
	v_lshl_add_u64 v[168:169], v[180:181], 0, v[166:167]
	v_lshl_add_u64 v[170:171], v[168:169], 0, s[2:3]
	v_lshl_add_u64 v[176:177], v[168:169], 0, s[38:39]
	global_load_dwordx4 v[168:171], v[170:171], off
	s_nop 0
	global_load_dwordx4 v[176:179], v[176:177], off
	v_lshl_add_u64 v[184:185], v[180:181], 0, s[2:3]
	v_lshl_add_u64 v[180:181], v[180:181], 0, s[38:39]
	v_lshl_add_u64 v[180:181], v[180:181], 0, v[4:5]
	global_load_dwordx4 v[180:183], v[180:181], off
	v_lshl_add_u64 v[184:185], v[184:185], 0, v[4:5]
	global_load_dwordx4 v[184:187], v[184:185], off
	s_waitcnt vmcnt(4)
	v_cvt_f32_f16_e32 v3, v226
	v_cvt_f32_f16_e32 v135, v230
	v_cvt_f32_f16_sdwa v155, v230 dst_sel:DWORD dst_unused:UNUSED_PAD src0_sel:WORD_1
	v_cvt_f32_f16_e32 v159, v231
	v_cvt_f32_f16_sdwa v153, v226 dst_sel:DWORD dst_unused:UNUSED_PAD src0_sel:WORD_1
	v_max_f32_e32 v135, 0x38d1b717, v135
	v_cvt_f32_f16_e32 v157, v227
	v_rcp_f32_e32 v135, v135
	v_cvt_f32_f16_sdwa v163, v231 dst_sel:DWORD dst_unused:UNUSED_PAD src0_sel:WORD_1
	v_cvt_f32_f16_e32 v230, v233
	v_cvt_f32_f16_sdwa v231, v233 dst_sel:DWORD dst_unused:UNUSED_PAD src0_sel:WORD_1
	v_cvt_f32_f16_e32 v233, v238
	v_cvt_f32_f16_sdwa v238, v238 dst_sel:DWORD dst_unused:UNUSED_PAD src0_sel:WORD_1
	v_max_f32_e32 v155, 0x38d1b717, v155
	v_max_f32_e32 v159, 0x38d1b717, v159
	v_max_f32_e32 v188, 0x38d1b717, v3
	v_rcp_f32_e32 v155, v155
	v_rcp_f32_e32 v159, v159
	v_cndmask_b32_e64 v3, v188, v3, s[0:1]
	v_cvt_f32_f16_sdwa v161, v227 dst_sel:DWORD dst_unused:UNUSED_PAD src0_sel:WORD_1
	v_cvt_f32_f16_e32 v165, v228
	v_cvt_f32_f16_e32 v226, v232
	v_cvt_f32_f16_sdwa v227, v228 dst_sel:DWORD dst_unused:UNUSED_PAD src0_sel:WORD_1
	v_cvt_f32_f16_sdwa v228, v232 dst_sel:DWORD dst_unused:UNUSED_PAD src0_sel:WORD_1
	v_cvt_f32_f16_e32 v232, v234
	v_cvt_f32_f16_sdwa v234, v234 dst_sel:DWORD dst_unused:UNUSED_PAD src0_sel:WORD_1
	v_max_f32_e32 v189, 0x38d1b717, v153
	v_max_f32_e32 v190, 0x38d1b717, v157
	v_mul_f32_e32 v3, v3, v135
	v_cndmask_b32_e64 v153, v189, v153, s[0:1]
	v_cndmask_b32_e64 v157, v190, v157, s[0:1]
	v_mul_f32_e32 v130, v130, v3
	v_max_f32_e32 v3, 0x38d1b717, v238
	v_mul_f32_e32 v135, v153, v155
	v_mul_f32_e32 v153, v157, v159
	v_rcp_f32_e32 v3, v3
	v_mul_f32_e32 v132, v132, v153
	v_cvt_f32_f16_e32 v153, v239
	v_mul_f32_e32 v131, v131, v135
	v_max_f32_e32 v135, 0x38d1b717, v234
	v_cndmask_b32_e64 v135, v135, v234, s[0:1]
	v_mul_f32_e32 v3, v135, v3
	v_cvt_f32_f16_e32 v135, v235
	v_mul_f32_e32 v123, v123, v3
	v_max_f32_e32 v3, 0x38d1b717, v153
	v_rcp_f32_e32 v3, v3
	v_max_f32_e32 v153, 0x38d1b717, v135
	v_cndmask_b32_e64 v135, v153, v135, s[0:1]
	v_cvt_f32_f16_sdwa v153, v239 dst_sel:DWORD dst_unused:UNUSED_PAD src0_sel:WORD_1
	v_mul_f32_e32 v3, v135, v3
	v_cvt_f32_f16_sdwa v135, v235 dst_sel:DWORD dst_unused:UNUSED_PAD src0_sel:WORD_1
	v_mul_f32_e32 v124, v124, v3
	v_max_f32_e32 v3, 0x38d1b717, v153
	v_rcp_f32_e32 v3, v3
	v_max_f32_e32 v153, 0x38d1b717, v135
	v_cndmask_b32_e64 v135, v153, v135, s[0:1]
	v_cvt_f32_f16_e32 v153, v240
	v_mul_f32_e32 v3, v135, v3
	v_cvt_f32_f16_e32 v135, v236
	v_mul_f32_e32 v125, v125, v3
	v_max_f32_e32 v3, 0x38d1b717, v153
	v_rcp_f32_e32 v3, v3
	v_max_f32_e32 v153, 0x38d1b717, v135
	v_cndmask_b32_e64 v135, v153, v135, s[0:1]
	v_cvt_f32_f16_sdwa v153, v240 dst_sel:DWORD dst_unused:UNUSED_PAD src0_sel:WORD_1
	v_mul_f32_e32 v3, v135, v3
	v_cvt_f32_f16_sdwa v135, v236 dst_sel:DWORD dst_unused:UNUSED_PAD src0_sel:WORD_1
	v_mul_f32_e32 v118, v118, v3
	v_max_f32_e32 v3, 0x38d1b717, v153
	v_rcp_f32_e32 v3, v3
	v_max_f32_e32 v153, 0x38d1b717, v135
	v_max_f32_e32 v163, 0x38d1b717, v163
	v_cndmask_b32_e64 v135, v153, v135, s[0:1]
	v_cvt_f32_f16_e32 v153, v241
	v_rcp_f32_e32 v163, v163
	v_max_f32_e32 v191, 0x38d1b717, v161
	v_mul_f32_e32 v3, v135, v3
	v_cvt_f32_f16_e32 v135, v237
	v_cndmask_b32_e64 v161, v191, v161, s[0:1]
	v_mul_f32_e32 v119, v119, v3
	v_max_f32_e32 v3, 0x38d1b717, v153
	v_mul_f32_e32 v155, v161, v163
	v_rcp_f32_e32 v3, v3
	v_mul_f32_e32 v133, v133, v155
	v_cvt_f32_f16_sdwa v155, v241 dst_sel:DWORD dst_unused:UNUSED_PAD src0_sel:WORD_1
	v_max_f32_e32 v153, 0x38d1b717, v135
	v_cndmask_b32_e64 v135, v153, v135, s[0:1]
	v_cvt_f32_f16_e32 v175, v229
	v_cvt_f32_f16_sdwa v229, v229 dst_sel:DWORD dst_unused:UNUSED_PAD src0_sel:WORD_1
	v_mul_f32_e32 v3, v135, v3
	v_cvt_f32_f16_sdwa v135, v237 dst_sel:DWORD dst_unused:UNUSED_PAD src0_sel:WORD_1
	v_max_f32_e32 v226, 0x38d1b717, v226
	v_max_f32_e32 v228, 0x38d1b717, v228
	v_max_f32_e32 v230, 0x38d1b717, v230
	v_max_f32_e32 v231, 0x38d1b717, v231
	v_max_f32_e32 v233, 0x38d1b717, v233
	v_max_f32_e32 v153, 0x38d1b717, v155
	v_rcp_f32_e32 v226, v226
	v_rcp_f32_e32 v228, v228
	v_rcp_f32_e32 v230, v230
	v_rcp_f32_e32 v231, v231
	v_rcp_f32_e32 v233, v233
	v_rcp_f32_e32 v153, v153
	v_max_f32_e32 v192, 0x38d1b717, v165
	v_max_f32_e32 v193, 0x38d1b717, v227
	v_max_f32_e32 v194, 0x38d1b717, v175
	v_max_f32_e32 v195, 0x38d1b717, v229
	v_max_f32_e32 v196, 0x38d1b717, v232
	v_mul_f32_e32 v120, v120, v3
	v_max_f32_e32 v3, 0x38d1b717, v135
	v_cndmask_b32_e64 v165, v192, v165, s[0:1]
	v_cndmask_b32_e64 v227, v193, v227, s[0:1]
	v_cndmask_b32_e64 v175, v194, v175, s[0:1]
	v_cndmask_b32_e64 v229, v195, v229, s[0:1]
	v_cndmask_b32_e64 v232, v196, v232, s[0:1]
	v_cndmask_b32_e64 v3, v3, v135, s[0:1]
	v_mul_f32_e32 v157, v165, v226
	v_mul_f32_e32 v159, v227, v228
	v_mul_f32_e32 v161, v175, v230
	v_mul_f32_e32 v163, v229, v231
	v_mul_f32_e32 v165, v232, v233
	v_mul_f32_e32 v3, v3, v153
	v_mul_f32_e32 v126, v126, v157
	v_mul_f32_e32 v127, v127, v159
	v_mul_f32_e32 v128, v128, v161
	v_mul_f32_e32 v129, v129, v163
	v_mul_f32_e32 v122, v122, v165
	v_mul_f32_e32 v121, v121, v3
	v_mov_b32_e32 v3, v162
	s_nop 0
	v_mad_i64_i32 v[226:227], s[40:41], v3, s62, v[136:137]
	v_lshl_add_u64 v[234:235], v[226:227], 0, s[16:17]
	v_lshl_add_u64 v[230:231], v[234:235], 0, v[166:167]
	v_lshl_add_u64 v[226:227], v[230:231], 0, s[38:39]
	global_load_dwordx4 v[226:229], v[226:227], off
	v_lshl_add_u64 v[230:231], v[230:231], 0, s[2:3]
	global_load_dwordx4 v[230:233], v[230:231], off
	v_lshl_add_u64 v[238:239], v[234:235], 0, s[2:3]
	v_lshl_add_u64 v[234:235], v[234:235], 0, s[38:39]
	v_lshl_add_u64 v[234:235], v[234:235], 0, v[4:5]
	global_load_dwordx4 v[234:237], v[234:235], off
	v_lshl_add_u64 v[238:239], v[238:239], 0, v[4:5]
	global_load_dwordx4 v[238:241], v[238:239], off
	s_waitcnt vmcnt(4)
	v_cvt_f32_f16_e32 v3, v168
	v_cvt_f32_f16_e32 v135, v176
	v_cvt_f32_f16_sdwa v155, v176 dst_sel:DWORD dst_unused:UNUSED_PAD src0_sel:WORD_1
	v_cvt_f32_f16_e32 v159, v177
	v_cvt_f32_f16_sdwa v153, v168 dst_sel:DWORD dst_unused:UNUSED_PAD src0_sel:WORD_1
	v_max_f32_e32 v135, 0x38d1b717, v135
	v_cvt_f32_f16_e32 v157, v169
	v_rcp_f32_e32 v135, v135
	v_cvt_f32_f16_sdwa v163, v177 dst_sel:DWORD dst_unused:UNUSED_PAD src0_sel:WORD_1
	v_max_f32_e32 v155, 0x38d1b717, v155
	v_max_f32_e32 v159, 0x38d1b717, v159
	v_max_f32_e32 v165, 0x38d1b717, v3
	v_rcp_f32_e32 v155, v155
	v_rcp_f32_e32 v159, v159
	v_cndmask_b32_e64 v3, v165, v3, s[0:1]
	v_cvt_f32_f16_sdwa v161, v169 dst_sel:DWORD dst_unused:UNUSED_PAD src0_sel:WORD_1
	v_max_f32_e32 v168, 0x38d1b717, v153
	v_max_f32_e32 v169, 0x38d1b717, v157
	v_mul_f32_e32 v3, v3, v135
	v_cndmask_b32_e64 v153, v168, v153, s[0:1]
	v_cndmask_b32_e64 v157, v169, v157, s[0:1]
	v_mul_f32_e32 v114, v114, v3
	v_max_f32_e32 v3, 0x38d1b717, v163
	v_mul_f32_e32 v135, v153, v155
	v_mul_f32_e32 v153, v157, v159
	v_rcp_f32_e32 v3, v3
	v_mul_f32_e32 v116, v116, v153
	v_cvt_f32_f16_e32 v153, v178
	v_mul_f32_e32 v115, v115, v135
	v_max_f32_e32 v135, 0x38d1b717, v161
	v_cndmask_b32_e64 v135, v135, v161, s[0:1]
	v_mul_f32_e32 v3, v135, v3
	v_cvt_f32_f16_e32 v135, v170
	v_mul_f32_e32 v117, v117, v3
	v_max_f32_e32 v3, 0x38d1b717, v153
	v_rcp_f32_e32 v3, v3
	v_max_f32_e32 v153, 0x38d1b717, v135
	v_cndmask_b32_e64 v135, v153, v135, s[0:1]
	v_cvt_f32_f16_sdwa v153, v178 dst_sel:DWORD dst_unused:UNUSED_PAD src0_sel:WORD_1
	v_mul_f32_e32 v3, v135, v3
	v_cvt_f32_f16_sdwa v135, v170 dst_sel:DWORD dst_unused:UNUSED_PAD src0_sel:WORD_1
	v_mul_f32_e32 v110, v110, v3
	v_max_f32_e32 v3, 0x38d1b717, v153
	v_rcp_f32_e32 v3, v3
	v_max_f32_e32 v153, 0x38d1b717, v135
	v_cndmask_b32_e64 v135, v153, v135, s[0:1]
	v_cvt_f32_f16_e32 v153, v179
	v_mul_f32_e32 v3, v135, v3
	v_cvt_f32_f16_e32 v135, v171
	v_mul_f32_e32 v111, v111, v3
	v_max_f32_e32 v3, 0x38d1b717, v153
	v_rcp_f32_e32 v3, v3
	v_max_f32_e32 v153, 0x38d1b717, v135
	v_cndmask_b32_e64 v135, v153, v135, s[0:1]
	v_cvt_f32_f16_sdwa v153, v179 dst_sel:DWORD dst_unused:UNUSED_PAD src0_sel:WORD_1
	v_mul_f32_e32 v3, v135, v3
	v_cvt_f32_f16_sdwa v135, v171 dst_sel:DWORD dst_unused:UNUSED_PAD src0_sel:WORD_1
	v_mul_f32_e32 v112, v112, v3
	v_max_f32_e32 v3, 0x38d1b717, v153
	v_rcp_f32_e32 v3, v3
	v_max_f32_e32 v153, 0x38d1b717, v135
	v_cndmask_b32_e64 v135, v153, v135, s[0:1]
	v_cvt_f32_f16_e32 v153, v180
	v_mul_f32_e32 v3, v135, v3
	v_cvt_f32_f16_e32 v135, v184
	v_mul_f32_e32 v113, v113, v3
	v_max_f32_e32 v3, 0x38d1b717, v153
	v_rcp_f32_e32 v3, v3
	v_max_f32_e32 v153, 0x38d1b717, v135
	v_cndmask_b32_e64 v135, v153, v135, s[0:1]
	v_cvt_f32_f16_sdwa v153, v180 dst_sel:DWORD dst_unused:UNUSED_PAD src0_sel:WORD_1
	v_mul_f32_e32 v3, v135, v3
	v_cvt_f32_f16_sdwa v135, v184 dst_sel:DWORD dst_unused:UNUSED_PAD src0_sel:WORD_1
	v_mul_f32_e32 v106, v106, v3
	v_max_f32_e32 v3, 0x38d1b717, v153
	v_rcp_f32_e32 v3, v3
	v_max_f32_e32 v153, 0x38d1b717, v135
	v_cndmask_b32_e64 v135, v153, v135, s[0:1]
	v_cvt_f32_f16_e32 v153, v181
	v_mul_f32_e32 v3, v135, v3
	v_cvt_f32_f16_e32 v135, v185
	v_mul_f32_e32 v107, v107, v3
	v_max_f32_e32 v3, 0x38d1b717, v153
	v_rcp_f32_e32 v3, v3
	v_max_f32_e32 v153, 0x38d1b717, v135
	v_cndmask_b32_e64 v135, v153, v135, s[0:1]
	v_cvt_f32_f16_sdwa v153, v181 dst_sel:DWORD dst_unused:UNUSED_PAD src0_sel:WORD_1
	v_mul_f32_e32 v3, v135, v3
	v_cvt_f32_f16_sdwa v135, v185 dst_sel:DWORD dst_unused:UNUSED_PAD src0_sel:WORD_1
	v_mul_f32_e32 v108, v108, v3
	v_max_f32_e32 v3, 0x38d1b717, v153
	v_rcp_f32_e32 v3, v3
	v_max_f32_e32 v153, 0x38d1b717, v135
	v_cndmask_b32_e64 v135, v153, v135, s[0:1]
	v_cvt_f32_f16_e32 v153, v182
	v_mul_f32_e32 v3, v135, v3
	v_cvt_f32_f16_e32 v135, v186
	v_mul_f32_e32 v109, v109, v3
	v_max_f32_e32 v3, 0x38d1b717, v153
	v_rcp_f32_e32 v3, v3
	v_max_f32_e32 v153, 0x38d1b717, v135
	v_cndmask_b32_e64 v135, v153, v135, s[0:1]
	v_cvt_f32_f16_sdwa v153, v182 dst_sel:DWORD dst_unused:UNUSED_PAD src0_sel:WORD_1
	v_mul_f32_e32 v3, v135, v3
	v_cvt_f32_f16_sdwa v135, v186 dst_sel:DWORD dst_unused:UNUSED_PAD src0_sel:WORD_1
	v_mul_f32_e32 v102, v102, v3
	v_max_f32_e32 v3, 0x38d1b717, v153
	v_rcp_f32_e32 v3, v3
	v_max_f32_e32 v153, 0x38d1b717, v135
	v_cndmask_b32_e64 v135, v153, v135, s[0:1]
	v_cvt_f32_f16_e32 v153, v183
	v_mul_f32_e32 v3, v135, v3
	v_cvt_f32_f16_e32 v135, v187
	v_mul_f32_e32 v103, v103, v3
	v_max_f32_e32 v3, 0x38d1b717, v153
	v_rcp_f32_e32 v3, v3
	v_cvt_f32_f16_sdwa v155, v183 dst_sel:DWORD dst_unused:UNUSED_PAD src0_sel:WORD_1
	v_max_f32_e32 v153, 0x38d1b717, v135
	v_cndmask_b32_e64 v135, v153, v135, s[0:1]
	v_mul_f32_e32 v3, v135, v3
	v_cvt_f32_f16_sdwa v135, v187 dst_sel:DWORD dst_unused:UNUSED_PAD src0_sel:WORD_1
	v_max_f32_e32 v153, 0x38d1b717, v155
	v_rcp_f32_e32 v153, v153
	v_mul_f32_e32 v104, v104, v3
	v_max_f32_e32 v3, 0x38d1b717, v135
	v_cndmask_b32_e64 v3, v3, v135, s[0:1]
	v_mul_f32_e32 v3, v3, v153
	v_mul_f32_e32 v105, v105, v3
	v_mov_b32_e32 v3, v160
	s_nop 0
	v_mad_i64_i32 v[168:169], s[40:41], v3, s62, v[136:137]
	v_lshl_add_u64 v[180:181], v[168:169], 0, s[16:17]
	v_lshl_add_u64 v[176:177], v[180:181], 0, v[166:167]
	v_lshl_add_u64 v[168:169], v[176:177], 0, s[38:39]
	global_load_dwordx4 v[168:171], v[168:169], off
	v_lshl_add_u64 v[176:177], v[176:177], 0, s[2:3]
	global_load_dwordx4 v[176:179], v[176:177], off
	v_lshl_add_u64 v[184:185], v[180:181], 0, s[2:3]
	v_lshl_add_u64 v[180:181], v[180:181], 0, s[38:39]
	v_lshl_add_u64 v[180:181], v[180:181], 0, v[4:5]
	global_load_dwordx4 v[180:183], v[180:181], off
	v_lshl_add_u64 v[184:185], v[184:185], 0, v[4:5]
	global_load_dwordx4 v[184:187], v[184:185], off
	s_waitcnt vmcnt(4)
	v_cvt_f32_f16_e32 v3, v226
	v_cvt_f32_f16_e32 v135, v230
	v_max_f32_e32 v3, 0x38d1b717, v3
	v_rcp_f32_e32 v3, v3
	v_max_f32_e32 v153, 0x38d1b717, v135
	v_cndmask_b32_e64 v135, v153, v135, s[0:1]
	v_cvt_f32_f16_sdwa v153, v226 dst_sel:DWORD dst_unused:UNUSED_PAD src0_sel:WORD_1
	v_mul_f32_e32 v3, v135, v3
	v_cvt_f32_f16_sdwa v135, v230 dst_sel:DWORD dst_unused:UNUSED_PAD src0_sel:WORD_1
	v_mul_f32_e32 v98, v98, v3
	v_max_f32_e32 v3, 0x38d1b717, v153
	v_rcp_f32_e32 v3, v3
	v_max_f32_e32 v153, 0x38d1b717, v135
	v_cndmask_b32_e64 v135, v153, v135, s[0:1]
	v_cvt_f32_f16_e32 v153, v227
	v_mul_f32_e32 v3, v135, v3
	v_cvt_f32_f16_e32 v135, v231
	v_mul_f32_e32 v99, v99, v3
	v_max_f32_e32 v3, 0x38d1b717, v153
	v_rcp_f32_e32 v3, v3
	v_max_f32_e32 v153, 0x38d1b717, v135
	v_cndmask_b32_e64 v135, v153, v135, s[0:1]
	v_cvt_f32_f16_sdwa v153, v227 dst_sel:DWORD dst_unused:UNUSED_PAD src0_sel:WORD_1
	v_mul_f32_e32 v3, v135, v3
	v_cvt_f32_f16_sdwa v135, v231 dst_sel:DWORD dst_unused:UNUSED_PAD src0_sel:WORD_1
	v_mul_f32_e32 v100, v100, v3
	v_max_f32_e32 v3, 0x38d1b717, v153
	v_rcp_f32_e32 v3, v3
	v_max_f32_e32 v153, 0x38d1b717, v135
	v_cndmask_b32_e64 v135, v153, v135, s[0:1]
	v_cvt_f32_f16_e32 v153, v228
	v_mul_f32_e32 v3, v135, v3
	v_cvt_f32_f16_e32 v135, v232
	v_mul_f32_e32 v101, v101, v3
	v_max_f32_e32 v3, 0x38d1b717, v153
	v_rcp_f32_e32 v3, v3
	v_max_f32_e32 v153, 0x38d1b717, v135
	v_cndmask_b32_e64 v135, v153, v135, s[0:1]
	v_cvt_f32_f16_sdwa v153, v228 dst_sel:DWORD dst_unused:UNUSED_PAD src0_sel:WORD_1
	v_mul_f32_e32 v3, v135, v3
	v_cvt_f32_f16_sdwa v135, v232 dst_sel:DWORD dst_unused:UNUSED_PAD src0_sel:WORD_1
	v_mul_f32_e32 v94, v94, v3
	v_max_f32_e32 v3, 0x38d1b717, v153
	v_rcp_f32_e32 v3, v3
	v_max_f32_e32 v153, 0x38d1b717, v135
	v_cndmask_b32_e64 v135, v153, v135, s[0:1]
	v_cvt_f32_f16_e32 v153, v229
	v_mul_f32_e32 v3, v135, v3
	v_cvt_f32_f16_e32 v135, v233
	v_mul_f32_e32 v95, v95, v3
	v_max_f32_e32 v3, 0x38d1b717, v153
	v_rcp_f32_e32 v3, v3
	v_max_f32_e32 v153, 0x38d1b717, v135
	v_cndmask_b32_e64 v135, v153, v135, s[0:1]
	v_cvt_f32_f16_sdwa v153, v229 dst_sel:DWORD dst_unused:UNUSED_PAD src0_sel:WORD_1
	v_mul_f32_e32 v3, v135, v3
	v_cvt_f32_f16_sdwa v135, v233 dst_sel:DWORD dst_unused:UNUSED_PAD src0_sel:WORD_1
	v_mul_f32_e32 v96, v96, v3
	v_max_f32_e32 v3, 0x38d1b717, v153
	v_rcp_f32_e32 v3, v3
	v_max_f32_e32 v153, 0x38d1b717, v135
	v_cndmask_b32_e64 v135, v153, v135, s[0:1]
	v_cvt_f32_f16_e32 v153, v234
	v_mul_f32_e32 v3, v135, v3
	v_cvt_f32_f16_e32 v135, v238
	v_mul_f32_e32 v97, v97, v3
	v_max_f32_e32 v3, 0x38d1b717, v153
	v_rcp_f32_e32 v3, v3
	v_max_f32_e32 v153, 0x38d1b717, v135
	v_cndmask_b32_e64 v135, v153, v135, s[0:1]
	v_cvt_f32_f16_sdwa v153, v234 dst_sel:DWORD dst_unused:UNUSED_PAD src0_sel:WORD_1
	v_mul_f32_e32 v3, v135, v3
	v_cvt_f32_f16_sdwa v135, v238 dst_sel:DWORD dst_unused:UNUSED_PAD src0_sel:WORD_1
	v_mul_f32_e32 v90, v90, v3
	v_max_f32_e32 v3, 0x38d1b717, v153
	v_rcp_f32_e32 v3, v3
	v_max_f32_e32 v153, 0x38d1b717, v135
	v_cndmask_b32_e64 v135, v153, v135, s[0:1]
	v_cvt_f32_f16_e32 v153, v235
	v_mul_f32_e32 v3, v135, v3
	v_cvt_f32_f16_e32 v135, v239
	v_mul_f32_e32 v91, v91, v3
	v_max_f32_e32 v3, 0x38d1b717, v153
	v_rcp_f32_e32 v3, v3
	v_max_f32_e32 v153, 0x38d1b717, v135
	v_cndmask_b32_e64 v135, v153, v135, s[0:1]
	v_cvt_f32_f16_sdwa v153, v235 dst_sel:DWORD dst_unused:UNUSED_PAD src0_sel:WORD_1
	v_mul_f32_e32 v3, v135, v3
	v_cvt_f32_f16_sdwa v135, v239 dst_sel:DWORD dst_unused:UNUSED_PAD src0_sel:WORD_1
	v_mul_f32_e32 v92, v92, v3
	v_max_f32_e32 v3, 0x38d1b717, v153
	v_rcp_f32_e32 v3, v3
	v_max_f32_e32 v153, 0x38d1b717, v135
	v_cndmask_b32_e64 v135, v153, v135, s[0:1]
	v_cvt_f32_f16_e32 v153, v236
	v_mul_f32_e32 v3, v135, v3
	v_cvt_f32_f16_e32 v135, v240
	v_mul_f32_e32 v93, v93, v3
	v_max_f32_e32 v3, 0x38d1b717, v153
	v_rcp_f32_e32 v3, v3
	v_max_f32_e32 v153, 0x38d1b717, v135
	v_cndmask_b32_e64 v135, v153, v135, s[0:1]
	v_cvt_f32_f16_sdwa v153, v236 dst_sel:DWORD dst_unused:UNUSED_PAD src0_sel:WORD_1
	v_mul_f32_e32 v3, v135, v3
	v_cvt_f32_f16_sdwa v135, v240 dst_sel:DWORD dst_unused:UNUSED_PAD src0_sel:WORD_1
	v_mul_f32_e32 v86, v86, v3
	v_max_f32_e32 v3, 0x38d1b717, v153
	v_rcp_f32_e32 v3, v3
	v_max_f32_e32 v153, 0x38d1b717, v135
	v_cndmask_b32_e64 v135, v153, v135, s[0:1]
	v_cvt_f32_f16_e32 v153, v237
	v_mul_f32_e32 v3, v135, v3
	v_cvt_f32_f16_e32 v135, v241
	v_mul_f32_e32 v87, v87, v3
	v_max_f32_e32 v3, 0x38d1b717, v153
	v_rcp_f32_e32 v3, v3
	v_cvt_f32_f16_sdwa v155, v237 dst_sel:DWORD dst_unused:UNUSED_PAD src0_sel:WORD_1
	v_max_f32_e32 v153, 0x38d1b717, v135
	v_cndmask_b32_e64 v135, v153, v135, s[0:1]
	v_mul_f32_e32 v3, v135, v3
	v_cvt_f32_f16_sdwa v135, v241 dst_sel:DWORD dst_unused:UNUSED_PAD src0_sel:WORD_1
	v_max_f32_e32 v153, 0x38d1b717, v155
	v_rcp_f32_e32 v153, v153
	v_mul_f32_e32 v88, v88, v3
	v_max_f32_e32 v3, 0x38d1b717, v135
	v_cndmask_b32_e64 v3, v3, v135, s[0:1]
	v_mul_f32_e32 v3, v3, v153
	v_mul_f32_e32 v89, v89, v3
	v_mov_b32_e32 v3, v158
	s_nop 0
	v_mad_i64_i32 v[226:227], s[40:41], v3, s62, v[136:137]
	v_lshl_add_u64 v[234:235], v[226:227], 0, s[16:17]
	v_lshl_add_u64 v[230:231], v[234:235], 0, v[166:167]
	v_lshl_add_u64 v[226:227], v[230:231], 0, s[38:39]
	global_load_dwordx4 v[226:229], v[226:227], off
	v_lshl_add_u64 v[230:231], v[230:231], 0, s[2:3]
	global_load_dwordx4 v[230:233], v[230:231], off
	v_lshl_add_u64 v[238:239], v[234:235], 0, s[2:3]
	v_lshl_add_u64 v[234:235], v[234:235], 0, s[38:39]
	v_lshl_add_u64 v[234:235], v[234:235], 0, v[4:5]
	global_load_dwordx4 v[234:237], v[234:235], off
	v_lshl_add_u64 v[238:239], v[238:239], 0, v[4:5]
	global_load_dwordx4 v[238:241], v[238:239], off
	s_waitcnt vmcnt(4)
	v_cvt_f32_f16_e32 v3, v168
	v_cvt_f32_f16_e32 v135, v176
	v_max_f32_e32 v3, 0x38d1b717, v3
	v_rcp_f32_e32 v3, v3
	v_max_f32_e32 v153, 0x38d1b717, v135
	v_cndmask_b32_e64 v135, v153, v135, s[0:1]
	v_cvt_f32_f16_sdwa v153, v168 dst_sel:DWORD dst_unused:UNUSED_PAD src0_sel:WORD_1
	v_mul_f32_e32 v3, v135, v3
	v_cvt_f32_f16_sdwa v135, v176 dst_sel:DWORD dst_unused:UNUSED_PAD src0_sel:WORD_1
	v_mul_f32_e32 v82, v82, v3
	v_max_f32_e32 v3, 0x38d1b717, v153
	v_rcp_f32_e32 v3, v3
	v_max_f32_e32 v153, 0x38d1b717, v135
	v_cndmask_b32_e64 v135, v153, v135, s[0:1]
	v_cvt_f32_f16_e32 v153, v169
	v_mul_f32_e32 v3, v135, v3
	v_cvt_f32_f16_e32 v135, v177
	v_mul_f32_e32 v83, v83, v3
	v_max_f32_e32 v3, 0x38d1b717, v153
	v_rcp_f32_e32 v3, v3
	v_max_f32_e32 v153, 0x38d1b717, v135
	v_cndmask_b32_e64 v135, v153, v135, s[0:1]
	v_cvt_f32_f16_sdwa v153, v169 dst_sel:DWORD dst_unused:UNUSED_PAD src0_sel:WORD_1
	v_mul_f32_e32 v3, v135, v3
	v_cvt_f32_f16_sdwa v135, v177 dst_sel:DWORD dst_unused:UNUSED_PAD src0_sel:WORD_1
	v_mul_f32_e32 v84, v84, v3
	v_max_f32_e32 v3, 0x38d1b717, v153
	v_rcp_f32_e32 v3, v3
	v_max_f32_e32 v153, 0x38d1b717, v135
	v_cndmask_b32_e64 v135, v153, v135, s[0:1]
	v_cvt_f32_f16_e32 v153, v170
	v_mul_f32_e32 v3, v135, v3
	v_cvt_f32_f16_e32 v135, v178
	v_mul_f32_e32 v85, v85, v3
	v_max_f32_e32 v3, 0x38d1b717, v153
	v_rcp_f32_e32 v3, v3
	v_max_f32_e32 v153, 0x38d1b717, v135
	v_cndmask_b32_e64 v135, v153, v135, s[0:1]
	v_cvt_f32_f16_sdwa v153, v170 dst_sel:DWORD dst_unused:UNUSED_PAD src0_sel:WORD_1
	v_mul_f32_e32 v3, v135, v3
	v_cvt_f32_f16_sdwa v135, v178 dst_sel:DWORD dst_unused:UNUSED_PAD src0_sel:WORD_1
	v_mul_f32_e32 v78, v78, v3
	v_max_f32_e32 v3, 0x38d1b717, v153
	v_rcp_f32_e32 v3, v3
	v_max_f32_e32 v153, 0x38d1b717, v135
	v_cndmask_b32_e64 v135, v153, v135, s[0:1]
	v_cvt_f32_f16_e32 v153, v171
	v_mul_f32_e32 v3, v135, v3
	v_cvt_f32_f16_e32 v135, v179
	v_mul_f32_e32 v79, v79, v3
	v_max_f32_e32 v3, 0x38d1b717, v153
	v_rcp_f32_e32 v3, v3
	v_max_f32_e32 v153, 0x38d1b717, v135
	v_cndmask_b32_e64 v135, v153, v135, s[0:1]
	v_cvt_f32_f16_sdwa v153, v171 dst_sel:DWORD dst_unused:UNUSED_PAD src0_sel:WORD_1
	v_mul_f32_e32 v3, v135, v3
	v_cvt_f32_f16_sdwa v135, v179 dst_sel:DWORD dst_unused:UNUSED_PAD src0_sel:WORD_1
	v_mul_f32_e32 v80, v80, v3
	v_max_f32_e32 v3, 0x38d1b717, v153
	v_rcp_f32_e32 v3, v3
	v_max_f32_e32 v153, 0x38d1b717, v135
	v_cndmask_b32_e64 v135, v153, v135, s[0:1]
	v_cvt_f32_f16_e32 v153, v180
	v_mul_f32_e32 v3, v135, v3
	v_cvt_f32_f16_e32 v135, v184
	v_mul_f32_e32 v81, v81, v3
	v_max_f32_e32 v3, 0x38d1b717, v153
	v_rcp_f32_e32 v3, v3
	v_max_f32_e32 v153, 0x38d1b717, v135
	v_cndmask_b32_e64 v135, v153, v135, s[0:1]
	v_cvt_f32_f16_sdwa v153, v180 dst_sel:DWORD dst_unused:UNUSED_PAD src0_sel:WORD_1
	v_mul_f32_e32 v3, v135, v3
	v_cvt_f32_f16_sdwa v135, v184 dst_sel:DWORD dst_unused:UNUSED_PAD src0_sel:WORD_1
	v_mul_f32_e32 v74, v74, v3
	v_max_f32_e32 v3, 0x38d1b717, v153
	v_rcp_f32_e32 v3, v3
	v_max_f32_e32 v153, 0x38d1b717, v135
	v_cndmask_b32_e64 v135, v153, v135, s[0:1]
	v_cvt_f32_f16_e32 v153, v181
	v_mul_f32_e32 v3, v135, v3
	v_cvt_f32_f16_e32 v135, v185
	v_mul_f32_e32 v75, v75, v3
	v_max_f32_e32 v3, 0x38d1b717, v153
	v_rcp_f32_e32 v3, v3
	v_max_f32_e32 v153, 0x38d1b717, v135
	v_cndmask_b32_e64 v135, v153, v135, s[0:1]
	v_cvt_f32_f16_sdwa v153, v181 dst_sel:DWORD dst_unused:UNUSED_PAD src0_sel:WORD_1
	v_mul_f32_e32 v3, v135, v3
	v_cvt_f32_f16_sdwa v135, v185 dst_sel:DWORD dst_unused:UNUSED_PAD src0_sel:WORD_1
	v_mul_f32_e32 v76, v76, v3
	v_max_f32_e32 v3, 0x38d1b717, v153
	v_rcp_f32_e32 v3, v3
	v_max_f32_e32 v153, 0x38d1b717, v135
	v_cndmask_b32_e64 v135, v153, v135, s[0:1]
	v_cvt_f32_f16_e32 v153, v182
	v_mul_f32_e32 v3, v135, v3
	v_cvt_f32_f16_e32 v135, v186
	v_mul_f32_e32 v77, v77, v3
	v_max_f32_e32 v3, 0x38d1b717, v153
	v_rcp_f32_e32 v3, v3
	v_max_f32_e32 v153, 0x38d1b717, v135
	v_cndmask_b32_e64 v135, v153, v135, s[0:1]
	v_cvt_f32_f16_sdwa v153, v182 dst_sel:DWORD dst_unused:UNUSED_PAD src0_sel:WORD_1
	v_mul_f32_e32 v3, v135, v3
	v_cvt_f32_f16_sdwa v135, v186 dst_sel:DWORD dst_unused:UNUSED_PAD src0_sel:WORD_1
	v_mul_f32_e32 v70, v70, v3
	v_max_f32_e32 v3, 0x38d1b717, v153
	v_rcp_f32_e32 v3, v3
	v_max_f32_e32 v153, 0x38d1b717, v135
	v_cndmask_b32_e64 v135, v153, v135, s[0:1]
	v_cvt_f32_f16_e32 v153, v183
	v_mul_f32_e32 v3, v135, v3
	v_cvt_f32_f16_e32 v135, v187
	v_mul_f32_e32 v71, v71, v3
	v_max_f32_e32 v3, 0x38d1b717, v153
	v_rcp_f32_e32 v3, v3
	v_cvt_f32_f16_sdwa v155, v183 dst_sel:DWORD dst_unused:UNUSED_PAD src0_sel:WORD_1
	v_max_f32_e32 v153, 0x38d1b717, v135
	v_cndmask_b32_e64 v135, v153, v135, s[0:1]
	v_mul_f32_e32 v3, v135, v3
	v_cvt_f32_f16_sdwa v135, v187 dst_sel:DWORD dst_unused:UNUSED_PAD src0_sel:WORD_1
	v_max_f32_e32 v153, 0x38d1b717, v155
	v_rcp_f32_e32 v153, v153
	v_mul_f32_e32 v72, v72, v3
	v_max_f32_e32 v3, 0x38d1b717, v135
	v_cndmask_b32_e64 v3, v3, v135, s[0:1]
	v_mul_f32_e32 v3, v3, v153
	v_mul_f32_e32 v73, v73, v3
	v_mov_b32_e32 v3, v156
	s_nop 0
	v_mad_i64_i32 v[168:169], s[40:41], v3, s62, v[136:137]
	v_lshl_add_u64 v[180:181], v[168:169], 0, s[16:17]
	v_lshl_add_u64 v[176:177], v[180:181], 0, v[166:167]
	v_lshl_add_u64 v[168:169], v[176:177], 0, s[38:39]
	global_load_dwordx4 v[168:171], v[168:169], off
	v_lshl_add_u64 v[176:177], v[176:177], 0, s[2:3]
	global_load_dwordx4 v[176:179], v[176:177], off
	v_lshl_add_u64 v[184:185], v[180:181], 0, s[2:3]
	v_lshl_add_u64 v[180:181], v[180:181], 0, s[38:39]
	v_lshl_add_u64 v[180:181], v[180:181], 0, v[4:5]
	global_load_dwordx4 v[180:183], v[180:181], off
	v_lshl_add_u64 v[184:185], v[184:185], 0, v[4:5]
	global_load_dwordx4 v[184:187], v[184:185], off
	s_waitcnt vmcnt(4)
	v_cvt_f32_f16_e32 v3, v226
	v_cvt_f32_f16_e32 v135, v230
	v_max_f32_e32 v3, 0x38d1b717, v3
	v_rcp_f32_e32 v3, v3
	v_max_f32_e32 v153, 0x38d1b717, v135
	v_cndmask_b32_e64 v135, v153, v135, s[0:1]
	v_cvt_f32_f16_sdwa v153, v226 dst_sel:DWORD dst_unused:UNUSED_PAD src0_sel:WORD_1
	v_mul_f32_e32 v3, v135, v3
	v_cvt_f32_f16_sdwa v135, v230 dst_sel:DWORD dst_unused:UNUSED_PAD src0_sel:WORD_1
	v_mul_f32_e32 v66, v66, v3
	v_max_f32_e32 v3, 0x38d1b717, v153
	v_rcp_f32_e32 v3, v3
	v_max_f32_e32 v153, 0x38d1b717, v135
	v_cndmask_b32_e64 v135, v153, v135, s[0:1]
	v_cvt_f32_f16_e32 v153, v227
	v_mul_f32_e32 v3, v135, v3
	v_cvt_f32_f16_e32 v135, v231
	v_mul_f32_e32 v67, v67, v3
	v_max_f32_e32 v3, 0x38d1b717, v153
	v_rcp_f32_e32 v3, v3
	v_max_f32_e32 v153, 0x38d1b717, v135
	v_cndmask_b32_e64 v135, v153, v135, s[0:1]
	v_cvt_f32_f16_sdwa v153, v227 dst_sel:DWORD dst_unused:UNUSED_PAD src0_sel:WORD_1
	v_mul_f32_e32 v3, v135, v3
	v_cvt_f32_f16_sdwa v135, v231 dst_sel:DWORD dst_unused:UNUSED_PAD src0_sel:WORD_1
	v_mul_f32_e32 v68, v68, v3
	v_max_f32_e32 v3, 0x38d1b717, v153
	v_rcp_f32_e32 v3, v3
	v_max_f32_e32 v153, 0x38d1b717, v135
	v_cndmask_b32_e64 v135, v153, v135, s[0:1]
	v_cvt_f32_f16_e32 v153, v228
	v_mul_f32_e32 v3, v135, v3
	v_cvt_f32_f16_e32 v135, v232
	v_mul_f32_e32 v69, v69, v3
	v_max_f32_e32 v3, 0x38d1b717, v153
	v_rcp_f32_e32 v3, v3
	v_max_f32_e32 v153, 0x38d1b717, v135
	v_cndmask_b32_e64 v135, v153, v135, s[0:1]
	v_cvt_f32_f16_sdwa v153, v228 dst_sel:DWORD dst_unused:UNUSED_PAD src0_sel:WORD_1
	v_mul_f32_e32 v3, v135, v3
	v_cvt_f32_f16_sdwa v135, v232 dst_sel:DWORD dst_unused:UNUSED_PAD src0_sel:WORD_1
	v_mul_f32_e32 v62, v62, v3
	v_max_f32_e32 v3, 0x38d1b717, v153
	v_rcp_f32_e32 v3, v3
	v_max_f32_e32 v153, 0x38d1b717, v135
	v_cndmask_b32_e64 v135, v153, v135, s[0:1]
	v_cvt_f32_f16_e32 v153, v229
	v_mul_f32_e32 v3, v135, v3
	v_cvt_f32_f16_e32 v135, v233
	v_mul_f32_e32 v63, v63, v3
	v_max_f32_e32 v3, 0x38d1b717, v153
	v_rcp_f32_e32 v3, v3
	v_max_f32_e32 v153, 0x38d1b717, v135
	v_cndmask_b32_e64 v135, v153, v135, s[0:1]
	v_cvt_f32_f16_sdwa v153, v229 dst_sel:DWORD dst_unused:UNUSED_PAD src0_sel:WORD_1
	v_mul_f32_e32 v3, v135, v3
	v_cvt_f32_f16_sdwa v135, v233 dst_sel:DWORD dst_unused:UNUSED_PAD src0_sel:WORD_1
	v_mul_f32_e32 v64, v64, v3
	v_max_f32_e32 v3, 0x38d1b717, v153
	v_rcp_f32_e32 v3, v3
	v_max_f32_e32 v153, 0x38d1b717, v135
	v_cndmask_b32_e64 v135, v153, v135, s[0:1]
	v_cvt_f32_f16_e32 v153, v234
	v_mul_f32_e32 v3, v135, v3
	v_cvt_f32_f16_e32 v135, v238
	v_mul_f32_e32 v65, v65, v3
	v_max_f32_e32 v3, 0x38d1b717, v153
	v_rcp_f32_e32 v3, v3
	v_max_f32_e32 v153, 0x38d1b717, v135
	v_cndmask_b32_e64 v135, v153, v135, s[0:1]
	v_cvt_f32_f16_sdwa v153, v234 dst_sel:DWORD dst_unused:UNUSED_PAD src0_sel:WORD_1
	v_mul_f32_e32 v3, v135, v3
	v_cvt_f32_f16_sdwa v135, v238 dst_sel:DWORD dst_unused:UNUSED_PAD src0_sel:WORD_1
	v_mul_f32_e32 v58, v58, v3
	v_max_f32_e32 v3, 0x38d1b717, v153
	v_rcp_f32_e32 v3, v3
	v_max_f32_e32 v153, 0x38d1b717, v135
	v_cndmask_b32_e64 v135, v153, v135, s[0:1]
	v_cvt_f32_f16_e32 v153, v235
	v_mul_f32_e32 v3, v135, v3
	v_cvt_f32_f16_e32 v135, v239
	v_mul_f32_e32 v59, v59, v3
	v_max_f32_e32 v3, 0x38d1b717, v153
	v_rcp_f32_e32 v3, v3
	v_max_f32_e32 v153, 0x38d1b717, v135
	v_cndmask_b32_e64 v135, v153, v135, s[0:1]
	v_cvt_f32_f16_sdwa v153, v235 dst_sel:DWORD dst_unused:UNUSED_PAD src0_sel:WORD_1
	v_mul_f32_e32 v3, v135, v3
	v_cvt_f32_f16_sdwa v135, v239 dst_sel:DWORD dst_unused:UNUSED_PAD src0_sel:WORD_1
	v_mul_f32_e32 v60, v60, v3
	v_max_f32_e32 v3, 0x38d1b717, v153
	v_rcp_f32_e32 v3, v3
	v_max_f32_e32 v153, 0x38d1b717, v135
	v_cndmask_b32_e64 v135, v153, v135, s[0:1]
	v_cvt_f32_f16_e32 v153, v236
	v_mul_f32_e32 v3, v135, v3
	v_cvt_f32_f16_e32 v135, v240
	v_mul_f32_e32 v61, v61, v3
	v_max_f32_e32 v3, 0x38d1b717, v153
	v_rcp_f32_e32 v3, v3
	v_max_f32_e32 v153, 0x38d1b717, v135
	v_cndmask_b32_e64 v135, v153, v135, s[0:1]
	v_cvt_f32_f16_sdwa v153, v236 dst_sel:DWORD dst_unused:UNUSED_PAD src0_sel:WORD_1
	v_mul_f32_e32 v3, v135, v3
	v_cvt_f32_f16_sdwa v135, v240 dst_sel:DWORD dst_unused:UNUSED_PAD src0_sel:WORD_1
	v_mul_f32_e32 v54, v54, v3
	v_max_f32_e32 v3, 0x38d1b717, v153
	v_rcp_f32_e32 v3, v3
	v_max_f32_e32 v153, 0x38d1b717, v135
	v_cndmask_b32_e64 v135, v153, v135, s[0:1]
	v_cvt_f32_f16_e32 v153, v237
	v_mul_f32_e32 v3, v135, v3
	v_cvt_f32_f16_e32 v135, v241
	v_mul_f32_e32 v55, v55, v3
	v_max_f32_e32 v3, 0x38d1b717, v153
	v_rcp_f32_e32 v3, v3
	v_cvt_f32_f16_sdwa v155, v237 dst_sel:DWORD dst_unused:UNUSED_PAD src0_sel:WORD_1
	v_max_f32_e32 v153, 0x38d1b717, v135
	v_cndmask_b32_e64 v135, v153, v135, s[0:1]
	v_mul_f32_e32 v3, v135, v3
	v_cvt_f32_f16_sdwa v135, v241 dst_sel:DWORD dst_unused:UNUSED_PAD src0_sel:WORD_1
	v_max_f32_e32 v153, 0x38d1b717, v155
	v_rcp_f32_e32 v153, v153
	v_mul_f32_e32 v56, v56, v3
	v_max_f32_e32 v3, 0x38d1b717, v135
	v_cndmask_b32_e64 v3, v3, v135, s[0:1]
	v_mul_f32_e32 v3, v3, v153
	v_mul_f32_e32 v57, v57, v3
	v_mov_b32_e32 v3, v154
	s_nop 0
	v_mad_i64_i32 v[226:227], s[40:41], v3, s62, v[136:137]
	v_lshl_add_u64 v[234:235], v[226:227], 0, s[16:17]
	v_lshl_add_u64 v[230:231], v[234:235], 0, v[166:167]
	v_lshl_add_u64 v[226:227], v[230:231], 0, s[38:39]
	global_load_dwordx4 v[226:229], v[226:227], off
	v_lshl_add_u64 v[230:231], v[230:231], 0, s[2:3]
	global_load_dwordx4 v[230:233], v[230:231], off
	v_lshl_add_u64 v[238:239], v[234:235], 0, s[2:3]
	v_lshl_add_u64 v[234:235], v[234:235], 0, s[38:39]
	v_lshl_add_u64 v[234:235], v[234:235], 0, v[4:5]
	global_load_dwordx4 v[234:237], v[234:235], off
	v_lshl_add_u64 v[238:239], v[238:239], 0, v[4:5]
	global_load_dwordx4 v[238:241], v[238:239], off
	s_waitcnt vmcnt(4)
	v_cvt_f32_f16_e32 v3, v168
	v_cvt_f32_f16_e32 v135, v176
	v_max_f32_e32 v3, 0x38d1b717, v3
	v_rcp_f32_e32 v3, v3
	v_max_f32_e32 v153, 0x38d1b717, v135
	v_cndmask_b32_e64 v135, v153, v135, s[0:1]
	v_cvt_f32_f16_sdwa v153, v168 dst_sel:DWORD dst_unused:UNUSED_PAD src0_sel:WORD_1
	v_mul_f32_e32 v3, v135, v3
	v_cvt_f32_f16_sdwa v135, v176 dst_sel:DWORD dst_unused:UNUSED_PAD src0_sel:WORD_1
	v_mul_f32_e32 v50, v50, v3
	v_max_f32_e32 v3, 0x38d1b717, v153
	v_rcp_f32_e32 v3, v3
	v_max_f32_e32 v153, 0x38d1b717, v135
	v_cndmask_b32_e64 v135, v153, v135, s[0:1]
	v_cvt_f32_f16_e32 v153, v169
	v_mul_f32_e32 v3, v135, v3
	v_cvt_f32_f16_e32 v135, v177
	v_mul_f32_e32 v51, v51, v3
	v_max_f32_e32 v3, 0x38d1b717, v153
	v_rcp_f32_e32 v3, v3
	v_max_f32_e32 v153, 0x38d1b717, v135
	v_cndmask_b32_e64 v135, v153, v135, s[0:1]
	v_cvt_f32_f16_sdwa v153, v169 dst_sel:DWORD dst_unused:UNUSED_PAD src0_sel:WORD_1
	v_mul_f32_e32 v3, v135, v3
	v_cvt_f32_f16_sdwa v135, v177 dst_sel:DWORD dst_unused:UNUSED_PAD src0_sel:WORD_1
	v_mul_f32_e32 v52, v52, v3
	v_max_f32_e32 v3, 0x38d1b717, v153
	v_rcp_f32_e32 v3, v3
	v_max_f32_e32 v153, 0x38d1b717, v135
	v_cndmask_b32_e64 v135, v153, v135, s[0:1]
	v_cvt_f32_f16_e32 v153, v170
	v_mul_f32_e32 v3, v135, v3
	v_cvt_f32_f16_e32 v135, v178
	v_mul_f32_e32 v53, v53, v3
	v_max_f32_e32 v3, 0x38d1b717, v153
	v_rcp_f32_e32 v3, v3
	v_max_f32_e32 v153, 0x38d1b717, v135
	v_cndmask_b32_e64 v135, v153, v135, s[0:1]
	v_cvt_f32_f16_sdwa v153, v170 dst_sel:DWORD dst_unused:UNUSED_PAD src0_sel:WORD_1
	v_mul_f32_e32 v3, v135, v3
	v_cvt_f32_f16_sdwa v135, v178 dst_sel:DWORD dst_unused:UNUSED_PAD src0_sel:WORD_1
	v_mul_f32_e32 v46, v46, v3
	v_max_f32_e32 v3, 0x38d1b717, v153
	v_rcp_f32_e32 v3, v3
	v_max_f32_e32 v153, 0x38d1b717, v135
	v_cndmask_b32_e64 v135, v153, v135, s[0:1]
	v_cvt_f32_f16_e32 v153, v171
	v_mul_f32_e32 v3, v135, v3
	v_cvt_f32_f16_e32 v135, v179
	v_mul_f32_e32 v47, v47, v3
	v_max_f32_e32 v3, 0x38d1b717, v153
	v_rcp_f32_e32 v3, v3
	v_max_f32_e32 v153, 0x38d1b717, v135
	v_cndmask_b32_e64 v135, v153, v135, s[0:1]
	v_cvt_f32_f16_sdwa v153, v171 dst_sel:DWORD dst_unused:UNUSED_PAD src0_sel:WORD_1
	v_mul_f32_e32 v3, v135, v3
	v_cvt_f32_f16_sdwa v135, v179 dst_sel:DWORD dst_unused:UNUSED_PAD src0_sel:WORD_1
	v_mul_f32_e32 v48, v48, v3
	v_max_f32_e32 v3, 0x38d1b717, v153
	v_rcp_f32_e32 v3, v3
	v_max_f32_e32 v153, 0x38d1b717, v135
	v_cndmask_b32_e64 v135, v153, v135, s[0:1]
	v_cvt_f32_f16_e32 v153, v180
	v_mul_f32_e32 v3, v135, v3
	v_cvt_f32_f16_e32 v135, v184
	v_mul_f32_e32 v49, v49, v3
	v_max_f32_e32 v3, 0x38d1b717, v153
	v_rcp_f32_e32 v3, v3
	v_max_f32_e32 v153, 0x38d1b717, v135
	v_cndmask_b32_e64 v135, v153, v135, s[0:1]
	v_cvt_f32_f16_sdwa v153, v180 dst_sel:DWORD dst_unused:UNUSED_PAD src0_sel:WORD_1
	v_mul_f32_e32 v3, v135, v3
	v_cvt_f32_f16_sdwa v135, v184 dst_sel:DWORD dst_unused:UNUSED_PAD src0_sel:WORD_1
	v_mul_f32_e32 v42, v42, v3
	v_max_f32_e32 v3, 0x38d1b717, v153
	v_rcp_f32_e32 v3, v3
	v_max_f32_e32 v153, 0x38d1b717, v135
	v_cndmask_b32_e64 v135, v153, v135, s[0:1]
	v_cvt_f32_f16_e32 v153, v181
	v_mul_f32_e32 v3, v135, v3
	v_cvt_f32_f16_e32 v135, v185
	v_mul_f32_e32 v43, v43, v3
	v_max_f32_e32 v3, 0x38d1b717, v153
	v_rcp_f32_e32 v3, v3
	v_max_f32_e32 v153, 0x38d1b717, v135
	v_cndmask_b32_e64 v135, v153, v135, s[0:1]
	v_cvt_f32_f16_sdwa v153, v181 dst_sel:DWORD dst_unused:UNUSED_PAD src0_sel:WORD_1
	v_mul_f32_e32 v3, v135, v3
	v_cvt_f32_f16_sdwa v135, v185 dst_sel:DWORD dst_unused:UNUSED_PAD src0_sel:WORD_1
	v_mul_f32_e32 v44, v44, v3
	v_max_f32_e32 v3, 0x38d1b717, v153
	v_rcp_f32_e32 v3, v3
	v_max_f32_e32 v153, 0x38d1b717, v135
	v_cndmask_b32_e64 v135, v153, v135, s[0:1]
	v_cvt_f32_f16_e32 v153, v182
	v_mul_f32_e32 v3, v135, v3
	v_cvt_f32_f16_e32 v135, v186
	v_mul_f32_e32 v45, v45, v3
	v_max_f32_e32 v3, 0x38d1b717, v153
	v_rcp_f32_e32 v3, v3
	v_max_f32_e32 v153, 0x38d1b717, v135
	v_cndmask_b32_e64 v135, v153, v135, s[0:1]
	v_cvt_f32_f16_sdwa v153, v182 dst_sel:DWORD dst_unused:UNUSED_PAD src0_sel:WORD_1
	v_mul_f32_e32 v3, v135, v3
	v_cvt_f32_f16_sdwa v135, v186 dst_sel:DWORD dst_unused:UNUSED_PAD src0_sel:WORD_1
	v_mul_f32_e32 v38, v38, v3
	v_max_f32_e32 v3, 0x38d1b717, v153
	v_rcp_f32_e32 v3, v3
	v_max_f32_e32 v153, 0x38d1b717, v135
	v_cndmask_b32_e64 v135, v153, v135, s[0:1]
	v_cvt_f32_f16_e32 v153, v183
	v_mul_f32_e32 v3, v135, v3
	v_cvt_f32_f16_e32 v135, v187
	v_mul_f32_e32 v39, v39, v3
	v_max_f32_e32 v3, 0x38d1b717, v153
	v_rcp_f32_e32 v3, v3
	v_cvt_f32_f16_sdwa v155, v183 dst_sel:DWORD dst_unused:UNUSED_PAD src0_sel:WORD_1
	v_max_f32_e32 v153, 0x38d1b717, v135
	v_cndmask_b32_e64 v135, v153, v135, s[0:1]
	v_mul_f32_e32 v3, v135, v3
	v_cvt_f32_f16_sdwa v135, v187 dst_sel:DWORD dst_unused:UNUSED_PAD src0_sel:WORD_1
	v_max_f32_e32 v153, 0x38d1b717, v155
	v_rcp_f32_e32 v153, v153
	v_mul_f32_e32 v40, v40, v3
	v_max_f32_e32 v3, 0x38d1b717, v135
	v_cndmask_b32_e64 v3, v3, v135, s[0:1]
	v_mul_f32_e32 v3, v3, v153
	v_mul_f32_e32 v41, v41, v3
	v_mov_b32_e32 v3, v152
	s_nop 0
	v_mad_i64_i32 v[136:137], s[40:41], v3, s62, v[136:137]
	v_lshl_add_u64 v[136:137], v[136:137], 0, s[16:17]
	v_lshl_add_u64 v[170:171], v[136:137], 0, v[166:167]
	v_lshl_add_u64 v[166:167], v[170:171], 0, s[38:39]
	global_load_dwordx4 v[166:169], v[166:167], off
	v_lshl_add_u64 v[170:171], v[170:171], 0, s[2:3]
	global_load_dwordx4 v[176:179], v[170:171], off
	v_lshl_add_u64 v[170:171], v[136:137], 0, s[2:3]
	v_lshl_add_u64 v[136:137], v[136:137], 0, s[38:39]
	v_lshl_add_u64 v[136:137], v[136:137], 0, v[4:5]
	global_load_dwordx4 v[180:183], v[136:137], off
	v_lshl_add_u64 v[4:5], v[170:171], 0, v[4:5]
	global_load_dwordx4 v[184:187], v[4:5], off
	s_waitcnt vmcnt(4)
	v_cvt_f32_f16_e32 v3, v226
	v_cvt_f32_f16_e32 v135, v230
	v_max_f32_e32 v3, 0x38d1b717, v3
	v_rcp_f32_e32 v3, v3
	v_max_f32_e32 v153, 0x38d1b717, v135
	v_cndmask_b32_e64 v135, v153, v135, s[0:1]
	v_cvt_f32_f16_sdwa v153, v226 dst_sel:DWORD dst_unused:UNUSED_PAD src0_sel:WORD_1
	v_mul_f32_e32 v3, v135, v3
	v_cvt_f32_f16_sdwa v135, v230 dst_sel:DWORD dst_unused:UNUSED_PAD src0_sel:WORD_1
	v_mul_f32_e32 v34, v34, v3
	v_max_f32_e32 v3, 0x38d1b717, v153
	v_rcp_f32_e32 v3, v3
	v_max_f32_e32 v153, 0x38d1b717, v135
	v_cndmask_b32_e64 v135, v153, v135, s[0:1]
	v_cvt_f32_f16_e32 v153, v227
	v_mul_f32_e32 v3, v135, v3
	v_cvt_f32_f16_e32 v135, v231
	v_mul_f32_e32 v35, v35, v3
	v_max_f32_e32 v3, 0x38d1b717, v153
	v_rcp_f32_e32 v3, v3
	v_max_f32_e32 v153, 0x38d1b717, v135
	v_cndmask_b32_e64 v135, v153, v135, s[0:1]
	v_cvt_f32_f16_sdwa v153, v227 dst_sel:DWORD dst_unused:UNUSED_PAD src0_sel:WORD_1
	v_mul_f32_e32 v3, v135, v3
	v_cvt_f32_f16_sdwa v135, v231 dst_sel:DWORD dst_unused:UNUSED_PAD src0_sel:WORD_1
	v_mul_f32_e32 v36, v36, v3
	v_max_f32_e32 v3, 0x38d1b717, v153
	v_rcp_f32_e32 v3, v3
	v_max_f32_e32 v153, 0x38d1b717, v135
	v_cndmask_b32_e64 v135, v153, v135, s[0:1]
	v_cvt_f32_f16_e32 v153, v228
	v_mul_f32_e32 v3, v135, v3
	v_cvt_f32_f16_e32 v135, v232
	v_mul_f32_e32 v37, v37, v3
	v_max_f32_e32 v3, 0x38d1b717, v153
	v_rcp_f32_e32 v3, v3
	v_max_f32_e32 v153, 0x38d1b717, v135
	v_cndmask_b32_e64 v135, v153, v135, s[0:1]
	v_cvt_f32_f16_sdwa v153, v228 dst_sel:DWORD dst_unused:UNUSED_PAD src0_sel:WORD_1
	v_mul_f32_e32 v3, v135, v3
	v_cvt_f32_f16_sdwa v135, v232 dst_sel:DWORD dst_unused:UNUSED_PAD src0_sel:WORD_1
	v_mul_f32_e32 v30, v30, v3
	v_max_f32_e32 v3, 0x38d1b717, v153
	v_rcp_f32_e32 v3, v3
	v_max_f32_e32 v153, 0x38d1b717, v135
	v_cndmask_b32_e64 v135, v153, v135, s[0:1]
	v_cvt_f32_f16_e32 v153, v229
	v_mul_f32_e32 v3, v135, v3
	v_cvt_f32_f16_e32 v135, v233
	v_mul_f32_e32 v31, v31, v3
	v_max_f32_e32 v3, 0x38d1b717, v153
	v_rcp_f32_e32 v3, v3
	v_max_f32_e32 v153, 0x38d1b717, v135
	v_cndmask_b32_e64 v135, v153, v135, s[0:1]
	v_cvt_f32_f16_sdwa v153, v229 dst_sel:DWORD dst_unused:UNUSED_PAD src0_sel:WORD_1
	v_mul_f32_e32 v3, v135, v3
	v_cvt_f32_f16_sdwa v135, v233 dst_sel:DWORD dst_unused:UNUSED_PAD src0_sel:WORD_1
	v_mul_f32_e32 v32, v32, v3
	v_max_f32_e32 v3, 0x38d1b717, v153
	v_rcp_f32_e32 v3, v3
	v_max_f32_e32 v153, 0x38d1b717, v135
	v_cndmask_b32_e64 v135, v153, v135, s[0:1]
	v_cvt_f32_f16_e32 v153, v234
	v_mul_f32_e32 v3, v135, v3
	v_cvt_f32_f16_e32 v135, v238
	v_mul_f32_e32 v33, v33, v3
	v_max_f32_e32 v3, 0x38d1b717, v153
	v_rcp_f32_e32 v3, v3
	v_max_f32_e32 v153, 0x38d1b717, v135
	v_cndmask_b32_e64 v135, v153, v135, s[0:1]
	v_cvt_f32_f16_sdwa v153, v234 dst_sel:DWORD dst_unused:UNUSED_PAD src0_sel:WORD_1
	v_mul_f32_e32 v3, v135, v3
	v_cvt_f32_f16_sdwa v135, v238 dst_sel:DWORD dst_unused:UNUSED_PAD src0_sel:WORD_1
	v_mul_f32_e32 v26, v26, v3
	v_max_f32_e32 v3, 0x38d1b717, v153
	v_rcp_f32_e32 v3, v3
	v_max_f32_e32 v153, 0x38d1b717, v135
	v_cndmask_b32_e64 v135, v153, v135, s[0:1]
	v_cvt_f32_f16_e32 v153, v235
	v_mul_f32_e32 v3, v135, v3
	v_cvt_f32_f16_e32 v135, v239
	v_mul_f32_e32 v27, v27, v3
	v_max_f32_e32 v3, 0x38d1b717, v153
	v_rcp_f32_e32 v3, v3
	v_max_f32_e32 v153, 0x38d1b717, v135
	v_cndmask_b32_e64 v135, v153, v135, s[0:1]
	v_cvt_f32_f16_sdwa v153, v235 dst_sel:DWORD dst_unused:UNUSED_PAD src0_sel:WORD_1
	v_mul_f32_e32 v3, v135, v3
	v_cvt_f32_f16_sdwa v135, v239 dst_sel:DWORD dst_unused:UNUSED_PAD src0_sel:WORD_1
	v_mul_f32_e32 v28, v28, v3
	v_max_f32_e32 v3, 0x38d1b717, v153
	v_rcp_f32_e32 v3, v3
	v_max_f32_e32 v153, 0x38d1b717, v135
	v_cndmask_b32_e64 v135, v153, v135, s[0:1]
	v_cvt_f32_f16_e32 v153, v236
	v_mul_f32_e32 v3, v135, v3
	v_cvt_f32_f16_e32 v135, v240
	v_mul_f32_e32 v29, v29, v3
	v_max_f32_e32 v3, 0x38d1b717, v153
	v_rcp_f32_e32 v3, v3
	v_max_f32_e32 v153, 0x38d1b717, v135
	v_cndmask_b32_e64 v135, v153, v135, s[0:1]
	v_cvt_f32_f16_sdwa v153, v236 dst_sel:DWORD dst_unused:UNUSED_PAD src0_sel:WORD_1
	v_mul_f32_e32 v3, v135, v3
	v_cvt_f32_f16_sdwa v135, v240 dst_sel:DWORD dst_unused:UNUSED_PAD src0_sel:WORD_1
	v_mul_f32_e32 v22, v22, v3
	v_max_f32_e32 v3, 0x38d1b717, v153
	v_rcp_f32_e32 v3, v3
	v_max_f32_e32 v153, 0x38d1b717, v135
	v_cndmask_b32_e64 v135, v153, v135, s[0:1]
	v_cvt_f32_f16_e32 v153, v237
	v_mul_f32_e32 v3, v135, v3
	v_cvt_f32_f16_e32 v135, v241
	v_mul_f32_e32 v23, v23, v3
	v_max_f32_e32 v3, 0x38d1b717, v153
	v_rcp_f32_e32 v3, v3
	v_cvt_f32_f16_sdwa v155, v237 dst_sel:DWORD dst_unused:UNUSED_PAD src0_sel:WORD_1
	v_max_f32_e32 v153, 0x38d1b717, v135
	v_cndmask_b32_e64 v135, v153, v135, s[0:1]
	v_mul_f32_e32 v3, v135, v3
	v_cvt_f32_f16_sdwa v135, v241 dst_sel:DWORD dst_unused:UNUSED_PAD src0_sel:WORD_1
	v_max_f32_e32 v153, 0x38d1b717, v155
	v_rcp_f32_e32 v153, v153
	v_mul_f32_e32 v24, v24, v3
	v_max_f32_e32 v3, 0x38d1b717, v135
	v_cndmask_b32_e64 v3, v3, v135, s[0:1]
	v_mul_f32_e32 v3, v3, v153
	v_mul_f32_e32 v25, v25, v3
	s_waitcnt vmcnt(0)
	v_cvt_f32_f16_e32 v3, v166
	v_cvt_f32_f16_e32 v4, v176
	v_max_f32_e32 v3, 0x38d1b717, v3
	v_rcp_f32_e32 v3, v3
	v_max_f32_e32 v5, 0x38d1b717, v4
	v_cndmask_b32_e64 v4, v5, v4, s[0:1]
	v_cvt_f32_f16_sdwa v5, v166 dst_sel:DWORD dst_unused:UNUSED_PAD src0_sel:WORD_1
	v_mul_f32_e32 v3, v4, v3
	v_cvt_f32_f16_sdwa v4, v176 dst_sel:DWORD dst_unused:UNUSED_PAD src0_sel:WORD_1
	v_mul_f32_e32 v18, v18, v3
	v_max_f32_e32 v3, 0x38d1b717, v5
	v_rcp_f32_e32 v3, v3
	v_max_f32_e32 v5, 0x38d1b717, v4
	v_cndmask_b32_e64 v4, v5, v4, s[0:1]
	v_cvt_f32_f16_e32 v5, v167
	v_mul_f32_e32 v3, v4, v3
	v_cvt_f32_f16_e32 v4, v177
	v_mul_f32_e32 v19, v19, v3
	v_max_f32_e32 v3, 0x38d1b717, v5
	v_rcp_f32_e32 v3, v3
	v_max_f32_e32 v5, 0x38d1b717, v4
	v_cndmask_b32_e64 v4, v5, v4, s[0:1]
	v_cvt_f32_f16_sdwa v5, v167 dst_sel:DWORD dst_unused:UNUSED_PAD src0_sel:WORD_1
	v_mul_f32_e32 v3, v4, v3
	v_cvt_f32_f16_sdwa v4, v177 dst_sel:DWORD dst_unused:UNUSED_PAD src0_sel:WORD_1
	v_mul_f32_e32 v20, v20, v3
	v_max_f32_e32 v3, 0x38d1b717, v5
	v_rcp_f32_e32 v3, v3
	v_max_f32_e32 v5, 0x38d1b717, v4
	v_cndmask_b32_e64 v4, v5, v4, s[0:1]
	v_cvt_f32_f16_e32 v5, v168
	v_mul_f32_e32 v3, v4, v3
	v_cvt_f32_f16_e32 v4, v178
	v_mul_f32_e32 v21, v21, v3
	v_max_f32_e32 v3, 0x38d1b717, v5
	v_rcp_f32_e32 v3, v3
	v_max_f32_e32 v5, 0x38d1b717, v4
	v_cndmask_b32_e64 v4, v5, v4, s[0:1]
	v_cvt_f32_f16_sdwa v5, v168 dst_sel:DWORD dst_unused:UNUSED_PAD src0_sel:WORD_1
	v_mul_f32_e32 v3, v4, v3
	v_cvt_f32_f16_sdwa v4, v178 dst_sel:DWORD dst_unused:UNUSED_PAD src0_sel:WORD_1
	v_mul_f32_e32 v14, v14, v3
	v_max_f32_e32 v3, 0x38d1b717, v5
	v_rcp_f32_e32 v3, v3
	v_max_f32_e32 v5, 0x38d1b717, v4
	v_cndmask_b32_e64 v4, v5, v4, s[0:1]
	v_cvt_f32_f16_e32 v5, v169
	v_mul_f32_e32 v3, v4, v3
	v_cvt_f32_f16_e32 v4, v179
	v_mul_f32_e32 v15, v15, v3
	v_max_f32_e32 v3, 0x38d1b717, v5
	v_rcp_f32_e32 v3, v3
	v_max_f32_e32 v5, 0x38d1b717, v4
	v_cndmask_b32_e64 v4, v5, v4, s[0:1]
	v_cvt_f32_f16_sdwa v5, v169 dst_sel:DWORD dst_unused:UNUSED_PAD src0_sel:WORD_1
	v_mul_f32_e32 v3, v4, v3
	v_cvt_f32_f16_sdwa v4, v179 dst_sel:DWORD dst_unused:UNUSED_PAD src0_sel:WORD_1
	v_mul_f32_e32 v16, v16, v3
	v_max_f32_e32 v3, 0x38d1b717, v5
	v_rcp_f32_e32 v3, v3
	v_max_f32_e32 v5, 0x38d1b717, v4
	v_cndmask_b32_e64 v4, v5, v4, s[0:1]
	v_cvt_f32_f16_e32 v5, v180
	v_mul_f32_e32 v3, v4, v3
	v_cvt_f32_f16_e32 v4, v184
	v_mul_f32_e32 v17, v17, v3
	v_max_f32_e32 v3, 0x38d1b717, v5
	v_rcp_f32_e32 v3, v3
	v_max_f32_e32 v5, 0x38d1b717, v4
	v_cndmask_b32_e64 v4, v5, v4, s[0:1]
	v_cvt_f32_f16_sdwa v5, v180 dst_sel:DWORD dst_unused:UNUSED_PAD src0_sel:WORD_1
	v_mul_f32_e32 v3, v4, v3
	v_cvt_f32_f16_sdwa v4, v184 dst_sel:DWORD dst_unused:UNUSED_PAD src0_sel:WORD_1
	v_mul_f32_e32 v10, v10, v3
	v_max_f32_e32 v3, 0x38d1b717, v5
	v_rcp_f32_e32 v3, v3
	v_max_f32_e32 v5, 0x38d1b717, v4
	v_cndmask_b32_e64 v4, v5, v4, s[0:1]
	v_cvt_f32_f16_e32 v5, v181
	v_mul_f32_e32 v3, v4, v3
	v_cvt_f32_f16_e32 v4, v185
	v_mul_f32_e32 v11, v11, v3
	v_max_f32_e32 v3, 0x38d1b717, v5
	v_rcp_f32_e32 v3, v3
	v_max_f32_e32 v5, 0x38d1b717, v4
	v_cndmask_b32_e64 v4, v5, v4, s[0:1]
	v_cvt_f32_f16_sdwa v5, v181 dst_sel:DWORD dst_unused:UNUSED_PAD src0_sel:WORD_1
	v_mul_f32_e32 v3, v4, v3
	v_cvt_f32_f16_sdwa v4, v185 dst_sel:DWORD dst_unused:UNUSED_PAD src0_sel:WORD_1
	v_mul_f32_e32 v12, v12, v3
	v_max_f32_e32 v3, 0x38d1b717, v5
	v_rcp_f32_e32 v3, v3
	v_max_f32_e32 v5, 0x38d1b717, v4
	v_cndmask_b32_e64 v4, v5, v4, s[0:1]
	v_cvt_f32_f16_e32 v5, v182
	v_mul_f32_e32 v3, v4, v3
	v_cvt_f32_f16_e32 v4, v186
	v_mul_f32_e32 v13, v13, v3
	v_max_f32_e32 v3, 0x38d1b717, v5
	v_rcp_f32_e32 v3, v3
	v_max_f32_e32 v5, 0x38d1b717, v4
	v_cndmask_b32_e64 v4, v5, v4, s[0:1]
	v_cvt_f32_f16_sdwa v5, v182 dst_sel:DWORD dst_unused:UNUSED_PAD src0_sel:WORD_1
	v_mul_f32_e32 v3, v4, v3
	v_cvt_f32_f16_sdwa v4, v186 dst_sel:DWORD dst_unused:UNUSED_PAD src0_sel:WORD_1
	v_mul_f32_e32 v6, v6, v3
	v_max_f32_e32 v3, 0x38d1b717, v5
	v_rcp_f32_e32 v3, v3
	v_max_f32_e32 v5, 0x38d1b717, v4
	v_cndmask_b32_e64 v4, v5, v4, s[0:1]
	v_cvt_f32_f16_e32 v5, v183
	v_mul_f32_e32 v3, v4, v3
	v_cvt_f32_f16_e32 v4, v187
	v_mul_f32_e32 v7, v7, v3
	v_max_f32_e32 v3, 0x38d1b717, v5
	v_rcp_f32_e32 v3, v3
	v_cvt_f32_f16_sdwa v135, v183 dst_sel:DWORD dst_unused:UNUSED_PAD src0_sel:WORD_1
	v_max_f32_e32 v5, 0x38d1b717, v4
	v_cndmask_b32_e64 v4, v5, v4, s[0:1]
	v_mul_f32_e32 v3, v4, v3
	v_cvt_f32_f16_sdwa v4, v187 dst_sel:DWORD dst_unused:UNUSED_PAD src0_sel:WORD_1
	v_max_f32_e32 v5, 0x38d1b717, v135
	v_rcp_f32_e32 v5, v5
	v_mul_f32_e32 v8, v8, v3
	v_max_f32_e32 v3, 0x38d1b717, v4
	v_cndmask_b32_e64 v3, v3, v4, s[0:1]
	v_mul_f32_e32 v3, v3, v5
	v_mul_f32_e32 v9, v9, v3
	s_branch .LBB0_5351

.LBB0_5359:
	v_mov_b32_e32 v238, s30
	v_min_u32_e32 v238, 2, v238
	v_lshlrev_b32_e32 v238, 11, v238
	v_add_u32_e32 v238, 0x1800, v238
	v_mov_b64_e32 v[226:227], s[8:9]
	v_lshlrev_b64 v[228:229], 1, v[148:149]
	v_lshlrev_b64 v[230:231], 1, v[150:151]
	v_add_co_u32_e32 v228, vcc, v228, v238
	v_addc_co_u32_e32 v229, vcc, 0, v229, vcc
	v_add_co_u32_e32 v230, vcc, v230, v238
	v_addc_co_u32_e32 v231, vcc, 0, v231, vcc
	v_mad_i64_i32 v[232:233], s[4:5], v134, s62, v[226:227]
	v_lshl_add_u64 v[234:235], v[232:233], 0, v[228:229]
	v_lshl_add_u64 v[236:237], v[232:233], 0, v[230:231]
	global_load_dword v213, v[234:235], off
	global_load_dword v213, v[236:237], off
	v_mad_i64_i32 v[232:233], s[4:5], v164, s62, v[226:227]
	v_lshl_add_u64 v[234:235], v[232:233], 0, v[228:229]
	v_lshl_add_u64 v[236:237], v[232:233], 0, v[230:231]
	global_load_dword v213, v[234:235], off
	global_load_dword v213, v[236:237], off
	v_mad_i64_i32 v[232:233], s[4:5], v162, s62, v[226:227]
	v_lshl_add_u64 v[234:235], v[232:233], 0, v[228:229]
	v_lshl_add_u64 v[236:237], v[232:233], 0, v[230:231]
	global_load_dword v213, v[234:235], off
	global_load_dword v213, v[236:237], off
	v_mad_i64_i32 v[232:233], s[4:5], v160, s62, v[226:227]
	v_lshl_add_u64 v[234:235], v[232:233], 0, v[228:229]
	v_lshl_add_u64 v[236:237], v[232:233], 0, v[230:231]
	global_load_dword v213, v[234:235], off
	global_load_dword v213, v[236:237], off
	v_mad_i64_i32 v[232:233], s[4:5], v158, s62, v[226:227]
	v_lshl_add_u64 v[234:235], v[232:233], 0, v[228:229]
	v_lshl_add_u64 v[236:237], v[232:233], 0, v[230:231]
	global_load_dword v213, v[234:235], off
	global_load_dword v213, v[236:237], off
	v_mad_i64_i32 v[232:233], s[4:5], v156, s62, v[226:227]
	v_lshl_add_u64 v[234:235], v[232:233], 0, v[228:229]
	v_lshl_add_u64 v[236:237], v[232:233], 0, v[230:231]
	global_load_dword v213, v[234:235], off
	global_load_dword v213, v[236:237], off
	v_mad_i64_i32 v[232:233], s[4:5], v154, s62, v[226:227]
	v_lshl_add_u64 v[234:235], v[232:233], 0, v[228:229]
	v_lshl_add_u64 v[236:237], v[232:233], 0, v[230:231]
	global_load_dword v213, v[234:235], off
	global_load_dword v213, v[236:237], off
	v_mad_i64_i32 v[232:233], s[4:5], v152, s62, v[226:227]
	v_lshl_add_u64 v[234:235], v[232:233], 0, v[228:229]
	v_lshl_add_u64 v[236:237], v[232:233], 0, v[230:231]
	global_load_dword v213, v[234:235], off
	global_load_dword v213, v[236:237], off
	s_cmp_lt_i32 s30, 0
	v_mov_b64_e32 v[4:5], s[8:9]
	v_ashrrev_i32_e32 v135, 31, v134
	s_cselect_b64 s[34:35], -1, 0
	s_cmp_eq_u32 s30, 0
	v_lshlrev_b64 v[168:169], 11, v[134:135]
	v_mad_i64_i32 v[166:167], s[4:5], v134, s62, v[4:5]
	s_cselect_b64 s[0:1], -1, 0
	s_mov_b64 s[4:5], -1
	s_and_b64 vcc, exec, s[34:35]
	v_lshl_add_u64 v[4:5], s[10:11], 0, v[168:169]
	s_cbranch_vccz .LBB0_5361
	v_lshl_add_u64 v[134:135], v[148:149], 1, v[166:167]
	v_add_co_u32_e32 v134, vcc, 0x2000, v134
	v_mov_b32_e32 v176, v131
	s_nop 0
	v_addc_co_u32_e32 v135, vcc, 0, v135, vcc
	global_load_dwordx4 v[134:137], v[134:135], off offset:2048
	v_mov_b32_e32 v177, v132
	v_pk_mov_b32 v[178:179], v[132:133], v[126:127] op_sel:[1,0]
	v_mov_b32_e32 v180, v127
	v_mov_b32_e32 v181, v128
	v_lshl_add_u64 v[170:171], s[10:11], 0, v[168:169]
	s_mov_b64 s[4:5], 0
	s_waitcnt vmcnt(0)
	v_cvt_f32_f16_e32 v3, v134
	v_cvt_f32_f16_sdwa v134, v134 dst_sel:DWORD dst_unused:UNUSED_PAD src0_sel:WORD_1
	v_cvt_f32_f16_e32 v153, v135
	v_cvt_f32_f16_sdwa v155, v135 dst_sel:DWORD dst_unused:UNUSED_PAD src0_sel:WORD_1
	v_cvt_f32_f16_e32 v157, v136
	v_cvt_f32_f16_sdwa v159, v136 dst_sel:DWORD dst_unused:UNUSED_PAD src0_sel:WORD_1
	v_cvt_f32_f16_e32 v161, v137
	v_cvt_f32_f16_sdwa v163, v137 dst_sel:DWORD dst_unused:UNUSED_PAD src0_sel:WORD_1
	v_max_f32_e32 v134, 0x38d1b717, v134
	v_max_f32_e32 v135, 0x38d1b717, v153
	v_max_f32_e32 v136, 0x38d1b717, v155
	v_max_f32_e32 v137, 0x38d1b717, v157
	v_max_f32_e32 v182, 0x38d1b717, v159
	v_max_f32_e32 v183, 0x38d1b717, v161
	v_max_f32_e32 v3, 0x38d1b717, v3
	v_pk_mul_f32 v[134:135], v[176:177], v[134:135]
	v_pk_mul_f32 v[136:137], v[178:179], v[136:137]
	v_pk_mul_f32 v[176:177], v[180:181], v[182:183]
	v_fma_mixlo_f16 v3, v130, v3, 0
	v_cvt_pk_f16_f32 v135, v134, v135
	v_cvt_pk_f16_f32 v136, v136, v137
	v_cvt_pk_f16_f32 v137, v176, v177
	v_max_f32_e32 v153, 0x38d1b717, v163
	v_pack_b32_f16 v134, v3, v135
	v_alignbit_b32 v135, v136, v135, 16
	v_alignbit_b32 v136, v137, v136, 16
	v_lshrrev_b32_e32 v137, 16, v137
	v_fma_mixhi_f16 v137, v129, v153, 0
